# LDS-read prefetch rescheduling of MLA and MoBA attention steps (K fragments in use order, V fragments above softmax), bit-identical dataflow
# baseline (speedup 1.0000x reference)
; template <int DQK, int KB>
; __device__ __forceinline__ void qkt(f32x16& p0, f32x16& p1, const char* K_lds, int r32, int hi, const bf16x8* qr) {
;     constexpr int ROWB = DQK * 2, SHM_K = 64 * ROWB;
;     p0 = f32x16{}; p1 = f32x16{};
;     const char* kb[4];
; #pragma unroll
;     for (int dd = 0; dd < 4; ++dd) kb[dd] = K_lds + KB * SHM_K + r32 * ROWB + (((dd * 16 + hi * 8) * 2) ^ ((r32 & 7) << 4));
; #pragma unroll
;     for (int d0 = 0; d0 < DQK / 16; ++d0) { const char* a = kb[d0 & 3] + (d0 >> 2) * 128;
;         bf16x8 b0 = *reinterpret_cast<const bf16x8*>(a);
;         bf16x8 b1 = *reinterpret_cast<const bf16x8*>(a + 32 * ROWB);
;         p0 = __builtin_amdgcn_mfma_f32_32x32x16_bf16(b0, qr[d0], p0, 0, 0, 0);
;         p1 = __builtin_amdgcn_mfma_f32_32x32x16_bf16(b1, qr[d0], p1, 0, 0, 0); }
; __device__ __forceinline__ void p4_moba_loop(Frame& F, const Args& A, const int qo, const bool cvmode) {
;     ...
;             { const bf16_t* qp = WSP(bf16_t, WS_P) + (size_t)(b * SEQ + pos) * NPROJ + h * 128 + hi * 8;
; #pragma unroll
;               for (int d0 = 0; d0 < 8; ++d0) qr[d0] = *(const bf16x8*)(qp + d0 * 16); }
;             const int ntile = own ? (tk >> 1) + 1 : 4;
;             const int qrel = pos - n * 256;
;             f32x16 o[4]; float m_reg = -1e30f, l_reg = 0.f;
; #pragma unroll
;             for (int d = 0; d < 4; ++d) o[d] = f32x16{};
.LBB0_548:
	s_or_b64 exec, exec, s[8:9]
	v_readlane_b32 s8, v255, 18
	v_subrev_u32_e32 v132, s77, v134
	s_nop 0
	v_add_u32_e32 v2, s8, v134
	s_movk_i32 s8, 0x2200
	v_mad_i64_i32 v[2:3], s[8:9], v2, s8, v[140:141]
	global_load_dwordx4 v[126:129], v[2:3], off
	global_load_dwordx4 v[122:125], v[2:3], off offset:32
	global_load_dwordx4 v[118:121], v[2:3], off offset:64
	global_load_dwordx4 v[114:117], v[2:3], off offset:96
	global_load_dwordx4 v[110:113], v[2:3], off offset:128
	global_load_dwordx4 v[106:109], v[2:3], off offset:160
	global_load_dwordx4 v[102:105], v[2:3], off offset:192
	global_load_dwordx4 v[98:101], v[2:3], off offset:224
	s_cmp_gt_u32 s80, 1
	ds_read_b128 v[190:193], v166
	ds_read_b128 v[194:197], v166 offset:8192
	ds_read_b128 v[198:201], v167
	ds_read_b128 v[202:205], v167 offset:8192
	ds_read_b128 v[206:209], v168
	ds_read_b128 v[210:213], v168 offset:8192
	ds_read_b128 v[214:217], v169
	ds_read_b128 v[218:221], v169 offset:8192
	ds_read_b128 v[222:225], v166 offset:128
	ds_read_b128 v[226:229], v166 offset:8320
	ds_read_b128 v[230:233], v167 offset:128
	ds_read_b128 v[234:237], v167 offset:8320
	ds_read_b128 v[238:241], v168 offset:128
	s_waitcnt vmcnt(7) lgkmcnt(12)
	v_mfma_f32_32x32x16_bf16 v[18:33], v[190:193], v[126:129], 0
	ds_read_b128 v[242:245], v168 offset:8320
	s_waitcnt lgkmcnt(12)
	v_mfma_f32_32x32x16_bf16 v[2:17], v[194:197], v[126:129], 0
	ds_read_b128 v[246:249], v169 offset:128
	s_waitcnt vmcnt(6) lgkmcnt(12)
	v_mfma_f32_32x32x16_bf16 v[18:33], v[198:201], v[122:125], v[18:33]
	ds_read_b128 v[250:253], v169 offset:8320
	s_waitcnt lgkmcnt(12)
	v_mfma_f32_32x32x16_bf16 v[2:17], v[202:205], v[122:125], v[2:17]
	s_waitcnt vmcnt(5) lgkmcnt(11)
	v_mfma_f32_32x32x16_bf16 v[18:33], v[206:209], v[118:121], v[18:33]
	s_waitcnt lgkmcnt(10)
	v_mfma_f32_32x32x16_bf16 v[2:17], v[210:213], v[118:121], v[2:17]
	s_waitcnt vmcnt(4) lgkmcnt(9)
	v_mfma_f32_32x32x16_bf16 v[18:33], v[214:217], v[114:117], v[18:33]
	s_waitcnt lgkmcnt(8)
	v_mfma_f32_32x32x16_bf16 v[2:17], v[218:221], v[114:117], v[2:17]
	s_waitcnt vmcnt(3) lgkmcnt(7)
	v_mfma_f32_32x32x16_bf16 v[18:33], v[222:225], v[110:113], v[18:33]
	s_waitcnt lgkmcnt(6)
	v_mfma_f32_32x32x16_bf16 v[2:17], v[226:229], v[110:113], v[2:17]
	s_waitcnt vmcnt(2) lgkmcnt(5)
	v_mfma_f32_32x32x16_bf16 v[18:33], v[230:233], v[106:109], v[18:33]
	s_waitcnt lgkmcnt(4)
	v_mfma_f32_32x32x16_bf16 v[2:17], v[234:237], v[106:109], v[2:17]
	s_waitcnt vmcnt(1) lgkmcnt(3)
	v_mfma_f32_32x32x16_bf16 v[18:33], v[238:241], v[102:105], v[18:33]
	s_waitcnt lgkmcnt(2)
	v_mfma_f32_32x32x16_bf16 v[2:17], v[242:245], v[102:105], v[2:17]
	s_waitcnt vmcnt(0) lgkmcnt(1)
	v_mfma_f32_32x32x16_bf16 v[18:33], v[246:249], v[98:101], v[18:33]
	v_mov_b32_e32 v34, v151
	s_nop 0
	v_mul_f32_e32 v36, v34, v155
	v_fma_f32 v42, v34, s34, v36
	v_fma_f32 v43, v34, s35, v36
	v_fma_f32 v44, v34, s2, v36
	v_fma_f32 v45, v34, s3, v36
	v_pk_fma_f32 v[46:47], v[34:35], s[36:37], v[36:37] op_sel_hi:[0,1,0]
	s_waitcnt lgkmcnt(0)
	s_waitcnt lgkmcnt(0)
	v_mfma_f32_32x32x16_bf16 v[2:17], v[250:253], v[98:101], v[2:17]
	v_mov_b32_e32 v41, v34
	v_mul_f32_e32 v38, 0x42000000, v34
	v_fma_f32 v40, 0, v34, v36
	v_fmac_f32_e32 v41, v41, v155
	v_fma_f32 v48, v34, s38, v36
	v_fma_f32 v49, v34, s39, v36
	v_pk_fma_f32 v[50:51], v[34:35], s[40:41], v[36:37] op_sel_hi:[0,1,0]
	v_pk_fma_f32 v[52:53], v[34:35], s[42:43], v[36:37] op_sel_hi:[0,1,0]
	v_pk_fma_f32 v[34:35], v[34:35], s[44:45], v[36:37] op_sel_hi:[0,1,0]
	v_pk_add_f32 v[32:33], v[32:33], v[34:35]
	v_pk_add_f32 v[28:29], v[28:29], v[50:51]
	v_pk_add_f32 v[26:27], v[26:27], v[48:49]
	v_pk_add_f32 v[24:25], v[24:25], v[46:47]
	v_pk_add_f32 v[22:23], v[22:23], v[44:45]
	v_pk_add_f32 v[20:21], v[20:21], v[42:43]
	v_pk_add_f32 v[54:55], v[38:39], v[42:43] op_sel_hi:[0,1]
	v_pk_add_f32 v[44:45], v[38:39], v[44:45] op_sel_hi:[0,1]
	v_pk_add_f32 v[42:43], v[38:39], v[46:47] op_sel_hi:[0,1]
	v_pk_add_f32 v[46:47], v[38:39], v[48:49] op_sel_hi:[0,1]
	v_pk_add_f32 v[48:49], v[38:39], v[50:51] op_sel_hi:[0,1]
	v_pk_add_f32 v[36:37], v[38:39], v[52:53] op_sel_hi:[0,1]
	v_pk_add_f32 v[34:35], v[38:39], v[34:35] op_sel_hi:[0,1]
	v_pk_add_f32 v[50:51], v[38:39], v[40:41] op_sel_hi:[0,1]
	v_pk_add_f32 v[30:31], v[30:31], v[52:53]
	v_pk_add_f32 v[18:19], v[18:19], v[40:41]
	v_pk_add_f32 v[34:35], v[16:17], v[34:35]
	v_pk_add_f32 v[36:37], v[14:15], v[36:37]
	v_pk_add_f32 v[38:39], v[12:13], v[48:49]
	v_pk_add_f32 v[40:41], v[10:11], v[46:47]
	v_pk_add_f32 v[42:43], v[8:9], v[42:43]
	v_pk_add_f32 v[44:45], v[6:7], v[44:45]
	v_pk_add_f32 v[46:47], v[4:5], v[54:55]
	v_pk_add_f32 v[48:49], v[2:3], v[50:51]
	s_cbranch_scc1 .LBB0_550
; __device__ __forceinline__ void mask_tile(f32x16& p0, f32x16& p1, int dq) {
;     const float NEG = -__builtin_inff();
; #pragma unroll
;     for (int r = 0; r < 16; ++r) {
;         const int c = (r & 3) + 8 * (r >> 2);
;         if (dq - c < 0) p0[r] = NEG;
;         if (dq - c - 32 < 0) p1[r] = NEG;
;     }
; }
	v_sub_u32_e32 v2, v132, v154
	v_cmp_gt_i32_e64 s[66:67], 26, v2
	v_cmp_gt_i32_e64 s[68:69], 27, v2
	v_cmp_gt_i32_e64 s[64:65], 25, v2
	s_and_b64 s[66:67], s[68:69], s[66:67]
	v_cmp_gt_i32_e64 s[62:63], 24, v2
	s_and_b64 s[64:65], s[66:67], s[64:65]
	v_cmp_gt_i32_e64 s[60:61], 19, v2
	s_and_b64 s[62:63], s[64:65], s[62:63]
	v_cmp_gt_i32_e64 s[58:59], 18, v2
	s_and_b64 s[60:61], s[62:63], s[60:61]
	v_cmp_gt_i32_e64 s[56:57], 17, v2
	s_and_b64 s[58:59], s[60:61], s[58:59]
	v_cmp_gt_i32_e64 s[54:55], 16, v2
	s_and_b64 s[56:57], s[58:59], s[56:57]
	v_cmp_gt_i32_e64 s[52:53], 11, v2
	s_and_b64 s[54:55], s[56:57], s[54:55]
	v_cmp_gt_i32_e64 s[50:51], 10, v2
	s_and_b64 s[52:53], s[54:55], s[52:53]
	v_cmp_gt_i32_e64 s[48:49], 9, v2
	s_and_b64 s[50:51], s[52:53], s[50:51]
	v_cmp_gt_i32_e64 s[46:47], 8, v2
	s_and_b64 s[48:49], s[50:51], s[48:49]
	v_cmp_gt_i32_e64 s[44:45], 3, v2
	s_and_b64 s[46:47], s[48:49], s[46:47]
	v_cmp_gt_i32_e64 s[42:43], 2, v2
	s_and_b64 s[44:45], s[46:47], s[44:45]
	v_cmp_gt_i32_e64 s[40:41], 1, v2
	s_and_b64 s[42:43], s[44:45], s[42:43]
	v_cmp_gt_i32_e64 s[38:39], 0, v2
	s_and_b64 s[40:41], s[42:43], s[40:41]
	s_and_b64 s[38:39], s[40:41], s[38:39]
	v_cmp_gt_i32_e64 s[36:37], 58, v2
	v_cndmask_b32_e64 v18, v18, v147, s[38:39]
	v_cmp_gt_i32_e64 s[38:39], 59, v2
	v_cmp_gt_i32_e64 s[34:35], 57, v2
	s_and_b64 s[36:37], s[38:39], s[36:37]
	v_cmp_gt_i32_e64 s[30:31], 56, v2
	s_and_b64 s[34:35], s[36:37], s[34:35]
	v_cmp_gt_i32_e64 s[28:29], 51, v2
	s_and_b64 s[30:31], s[34:35], s[30:31]
	v_cmp_gt_i32_e64 s[26:27], 50, v2
	s_and_b64 s[28:29], s[30:31], s[28:29]
	v_cmp_gt_i32_e64 s[24:25], 49, v2
	s_and_b64 s[26:27], s[28:29], s[26:27]
	v_cmp_gt_i32_e64 s[22:23], 48, v2
	s_and_b64 s[24:25], s[26:27], s[24:25]
	v_cmp_gt_i32_e64 s[20:21], 43, v2
	s_and_b64 s[22:23], s[24:25], s[22:23]
	v_cmp_gt_i32_e64 s[18:19], 42, v2
	s_and_b64 s[20:21], s[22:23], s[20:21]
	v_cmp_gt_i32_e64 s[16:17], 41, v2
	s_and_b64 s[18:19], s[20:21], s[18:19]
	v_cmp_gt_i32_e64 s[14:15], 40, v2
	s_and_b64 s[16:17], s[18:19], s[16:17]
	v_cmp_gt_i32_e64 s[12:13], 35, v2
	s_and_b64 s[14:15], s[16:17], s[14:15]
	v_cmp_gt_i32_e64 s[10:11], 34, v2
	s_and_b64 s[12:13], s[14:15], s[12:13]
	v_cmp_gt_i32_e64 s[8:9], 33, v2
	s_and_b64 s[10:11], s[12:13], s[10:11]
	v_cmp_gt_i32_e32 vcc, 32, v2
	s_and_b64 s[8:9], s[10:11], s[8:9]
	v_cndmask_b32_e64 v21, v21, v147, s[44:45]
	s_mov_b32 s44, 0x41d00000
	v_cndmask_b32_e64 v20, v20, v147, s[42:43]
	s_mov_b32 s42, 0x41c00000
	v_cndmask_b32_e64 v19, v19, v147, s[40:41]
	s_mov_b32 s40, 0x41900000
	v_cndmask_b32_e64 v35, v35, v147, s[38:39]
	s_mov_b32 s38, 0x41800000
	v_cndmask_b32_e64 v34, v34, v147, s[36:37]
	s_mov_b32 s36, 0x41200000
	v_cndmask_b32_e64 v37, v37, v147, s[34:35]
	s_mov_b32 s34, 2.0
	s_and_b64 vcc, s[8:9], vcc
	v_cndmask_b32_e64 v33, v33, v147, s[68:69]
	v_cndmask_b32_e64 v32, v32, v147, s[66:67]
	v_cndmask_b32_e64 v31, v31, v147, s[64:65]
	v_cndmask_b32_e64 v30, v30, v147, s[62:63]
	v_cndmask_b32_e64 v29, v29, v147, s[60:61]
	v_cndmask_b32_e64 v28, v28, v147, s[58:59]
	v_cndmask_b32_e64 v27, v27, v147, s[56:57]
	v_cndmask_b32_e64 v26, v26, v147, s[54:55]
	v_cndmask_b32_e64 v25, v25, v147, s[52:53]
	v_cndmask_b32_e64 v24, v24, v147, s[50:51]
	v_cndmask_b32_e64 v23, v23, v147, s[48:49]
	v_cndmask_b32_e64 v22, v22, v147, s[46:47]
	s_mov_b32 s45, 0x41d80000
	s_mov_b32 s43, 0x41c80000
	s_mov_b32 s41, 0x41980000
	s_mov_b32 s39, 0x41880000
	s_mov_b32 s37, 0x41300000
	s_mov_b32 s35, 0x40400000
	v_cndmask_b32_e64 v36, v36, v147, s[30:31]
	v_cndmask_b32_e64 v39, v39, v147, s[28:29]
	v_cndmask_b32_e64 v38, v38, v147, s[26:27]
	v_cndmask_b32_e64 v41, v41, v147, s[24:25]
	v_cndmask_b32_e64 v40, v40, v147, s[22:23]
	v_cndmask_b32_e64 v43, v43, v147, s[20:21]
	v_cndmask_b32_e64 v42, v42, v147, s[18:19]
	v_cndmask_b32_e64 v45, v45, v147, s[16:17]
	v_cndmask_b32_e64 v44, v44, v147, s[14:15]
	v_cndmask_b32_e64 v47, v47, v147, s[12:13]
	v_cndmask_b32_e64 v46, v46, v147, s[10:11]
	v_cndmask_b32_e64 v49, v49, v147, s[8:9]
	v_cndmask_b32_e32 v48, v48, v147, vcc

; template <int DQK> __device__ __forceinline__ void partialSM(f32x16& p0, f32x16& p1, float& m_reg, float& mn, float& alpha) {
;     ...
;     for (int r = 0; r < 16; ++r) p0[r] = fmaf(p0[r], C2, mnL);
; #pragma unroll
;     for (int r = 0; r < 16; ++r) p1[r] = fmaf(p1[r], C2, mnL);
; #pragma unroll
;     for (int r = 0; r < 16; ++r) p0[r] = __builtin_amdgcn_exp2f(p0[r]);
; }
; __device__ __forceinline__ void finishSM(f32x16& p0, f32x16& p1, float alpha, float& l_reg, bf16x8& pa0, bf16x8& pa1, bf16x8& pa2, bf16x8& pa3) {
; #pragma unroll
;     for (int r = 0; r < 16; ++r) p1[r] = __builtin_amdgcn_exp2f(p1[r]);
;     float ps = 0;
; #pragma unroll
;     for (int r = 0; r < 16; ++r) ps += p0[r];
; #pragma unroll
;     for (int r = 0; r < 16; ++r) ps += p1[r];
;     { auto rr = __builtin_amdgcn_permlane32_swap(__float_as_uint(ps), __float_as_uint(ps), false, false);
;       ps = __uint_as_float(rr[0]) + __uint_as_float(rr[1]); }
;     l_reg = l_reg * alpha + ps;
;     ...
;     PK4(p0, 0, pa0); PK4(p0, 8, pa1); PK4(p1, 0, pa2); PK4(p1, 8, pa3);
;     ...
; }
; template <int VB>
; __device__ __forceinline__ void pv_tile(f32x16* o, int vb0, bf16x8 pa0, bf16x8 pa1, bf16x8 pa2, bf16x8 pa3) {
;     ...
;     PV_D0(0); PV_D0(1); PV_D0(2); PV_D0(3);
.LBB0_559:
	ds_read_b64_tr_b16 v[190:191], v152 offset:0
	ds_read_b64_tr_b16 v[192:193], v152 offset:2048
	ds_read_b64_tr_b16 v[194:195], v152 offset:4096
	ds_read_b64_tr_b16 v[196:197], v152 offset:6144
	ds_read_b64_tr_b16 v[198:199], v152 offset:8192
	ds_read_b64_tr_b16 v[200:201], v152 offset:10240
	ds_read_b64_tr_b16 v[202:203], v152 offset:12288
	ds_read_b64_tr_b16 v[204:205], v152 offset:14336
	ds_read_b64_tr_b16 v[206:207], v152 offset:512
	ds_read_b64_tr_b16 v[208:209], v152 offset:2560
	ds_read_b64_tr_b16 v[210:211], v152 offset:4608
	ds_read_b64_tr_b16 v[212:213], v152 offset:6656
	ds_read_b64_tr_b16 v[214:215], v152 offset:8704
	ds_read_b64_tr_b16 v[216:217], v152 offset:10752
	v_cndmask_b32_e64 v137, v148, v51, s[8:9]
	v_mul_f32_e32 v51, 0xbe0293ee, v137
	v_fmamk_f32 v18, v18, 0x3e0293ee, v51
	v_fmamk_f32 v19, v19, 0x3e0293ee, v51
	v_exp_f32_e32 v18, v18
	v_fmamk_f32 v20, v20, 0x3e0293ee, v51
	v_exp_f32_e32 v19, v19
	v_fmamk_f32 v21, v21, 0x3e0293ee, v51
	v_exp_f32_e32 v20, v20
	v_fmamk_f32 v22, v22, 0x3e0293ee, v51
	v_fmamk_f32 v23, v23, 0x3e0293ee, v51
	v_fmamk_f32 v24, v24, 0x3e0293ee, v51
	v_fmamk_f32 v25, v25, 0x3e0293ee, v51
	v_fmamk_f32 v26, v26, 0x3e0293ee, v51
	v_fmamk_f32 v27, v27, 0x3e0293ee, v51
	v_fmamk_f32 v28, v28, 0x3e0293ee, v51
	v_fmamk_f32 v29, v29, 0x3e0293ee, v51
	v_fmamk_f32 v30, v30, 0x3e0293ee, v51
	v_fmamk_f32 v31, v31, 0x3e0293ee, v51
	v_fmamk_f32 v32, v32, 0x3e0293ee, v51
	v_fmamk_f32 v33, v33, 0x3e0293ee, v51
	v_fmamk_f32 v48, v48, 0x3e0293ee, v51
	v_fmamk_f32 v49, v49, 0x3e0293ee, v51
	v_fmamk_f32 v46, v46, 0x3e0293ee, v51
	v_fmamk_f32 v47, v47, 0x3e0293ee, v51
	v_fmamk_f32 v44, v44, 0x3e0293ee, v51
	v_fmamk_f32 v45, v45, 0x3e0293ee, v51
	v_fmamk_f32 v42, v42, 0x3e0293ee, v51
	v_fmamk_f32 v43, v43, 0x3e0293ee, v51
	v_fmamk_f32 v40, v40, 0x3e0293ee, v51
	v_fmamk_f32 v41, v41, 0x3e0293ee, v51
	v_fmamk_f32 v38, v38, 0x3e0293ee, v51
	v_fmamk_f32 v39, v39, 0x3e0293ee, v51
	v_fmamk_f32 v36, v36, 0x3e0293ee, v51
	v_fmamk_f32 v37, v37, 0x3e0293ee, v51
	v_fmamk_f32 v34, v34, 0x3e0293ee, v51
	v_fmac_f32_e32 v51, 0x3e0293ee, v35
	v_exp_f32_e32 v21, v21
	v_exp_f32_e32 v22, v22
	v_exp_f32_e32 v35, v48
	v_exp_f32_e32 v48, v49
	v_exp_f32_e32 v49, v51
	v_add_f32_e32 v51, 0, v18
	v_exp_f32_e32 v23, v23
	v_add_f32_e32 v51, v19, v51
	v_exp_f32_e32 v24, v24
	v_add_f32_e32 v51, v20, v51
	v_exp_f32_e32 v25, v25
	v_add_f32_e32 v51, v21, v51
	v_exp_f32_e32 v26, v26
	v_add_f32_e32 v51, v22, v51
	v_exp_f32_e32 v27, v27
	v_add_f32_e32 v51, v23, v51
	v_exp_f32_e32 v28, v28
	v_add_f32_e32 v51, v24, v51
	v_exp_f32_e32 v29, v29
	v_add_f32_e32 v51, v25, v51
	v_exp_f32_e32 v30, v30
	v_add_f32_e32 v51, v26, v51
	v_exp_f32_e32 v31, v31
	v_add_f32_e32 v51, v27, v51
	v_exp_f32_e32 v32, v32
	v_add_f32_e32 v51, v28, v51
	v_exp_f32_e32 v33, v33
	v_add_f32_e32 v51, v29, v51
	v_add_f32_e32 v51, v30, v51
	v_add_f32_e32 v51, v31, v51
	v_exp_f32_e32 v46, v46
	v_add_f32_e32 v51, v32, v51
	v_exp_f32_e32 v47, v47
	v_add_f32_e32 v51, v33, v51
	v_exp_f32_e32 v44, v44
	v_add_f32_e32 v51, v35, v51
	v_exp_f32_e32 v45, v45
	v_add_f32_e32 v51, v48, v51
	v_exp_f32_e32 v42, v42
	v_add_f32_e32 v51, v46, v51
	v_exp_f32_e32 v43, v43
	v_add_f32_e32 v51, v47, v51
	v_exp_f32_e32 v40, v40
	v_add_f32_e32 v51, v44, v51
	v_exp_f32_e32 v41, v41
	v_add_f32_e32 v51, v45, v51
	v_exp_f32_e32 v38, v38
	v_add_f32_e32 v51, v42, v51
	v_exp_f32_e32 v39, v39
	v_add_f32_e32 v51, v43, v51
	v_exp_f32_e32 v36, v36
	v_add_f32_e32 v51, v40, v51
	v_exp_f32_e32 v37, v37
	v_add_f32_e32 v51, v41, v51
	v_exp_f32_e32 v34, v34
	v_add_f32_e32 v51, v38, v51
	v_add_f32_e32 v51, v39, v51
	v_add_f32_e32 v51, v36, v51
	v_add_f32_e32 v51, v37, v51
	v_add_f32_e32 v51, v34, v51
	v_add_f32_e32 v51, v49, v51
	v_mov_b32_e32 v52, v51
	s_nop 1
	v_permlane32_swap_b32_e32 v51, v52
	s_and_b64 s[8:9], s[74:75], exec
	v_add_f32_e32 v145, v51, v52
	s_cselect_b32 s33, s81, 4
	v_fmac_f32_e32 v145, 0, v50
	v_cvt_pk_bf16_f32 v66, v18, v19
	v_cvt_pk_bf16_f32 v67, v20, v21
	v_cvt_pk_bf16_f32 v68, v22, v23
	v_cvt_pk_bf16_f32 v69, v24, v25
	v_cvt_pk_bf16_f32 v70, v26, v27
	v_cvt_pk_bf16_f32 v71, v28, v29
	v_cvt_pk_bf16_f32 v72, v30, v31
	v_cvt_pk_bf16_f32 v73, v32, v33
	v_cvt_pk_bf16_f32 v74, v35, v48
	v_cvt_pk_bf16_f32 v75, v46, v47
	v_cvt_pk_bf16_f32 v76, v44, v45
	v_cvt_pk_bf16_f32 v77, v42, v43
	v_cvt_pk_bf16_f32 v78, v40, v41
	v_cvt_pk_bf16_f32 v79, v38, v39
	v_cvt_pk_bf16_f32 v80, v36, v37
	v_cvt_pk_bf16_f32 v81, v34, v49
	s_nop 0
	v_permlane32_swap_b32_e32 v66, v68
	v_permlane32_swap_b32_e32 v67, v69
	v_permlane32_swap_b32_e32 v70, v72
	v_permlane32_swap_b32_e32 v71, v73
	v_permlane32_swap_b32_e32 v74, v76
	v_permlane32_swap_b32_e32 v75, v77
	v_permlane32_swap_b32_e32 v78, v80
	v_permlane32_swap_b32_e32 v79, v81
	s_waitcnt lgkmcnt(0)
	ds_read_b64_tr_b16 v[218:219], v152 offset:12800
	ds_read_b64_tr_b16 v[220:221], v152 offset:14848
	ds_read_b64_tr_b16 v[222:223], v152 offset:1024
	ds_read_b64_tr_b16 v[224:225], v152 offset:3072
	ds_read_b64_tr_b16 v[226:227], v152 offset:5120
	ds_read_b64_tr_b16 v[228:229], v152 offset:7168
	ds_read_b64_tr_b16 v[230:231], v152 offset:9216
	ds_read_b64_tr_b16 v[232:233], v152 offset:11264
	v_mfma_f32_32x32x16_bf16 v[18:33], v[66:69], v[190:193], v[2:17]
	ds_read_b64_tr_b16 v[190:191], v152 offset:13312
	ds_read_b64_tr_b16 v[192:193], v152 offset:15360
	v_mfma_f32_32x32x16_bf16 v[18:33], v[70:73], v[194:197], v[18:33]
	ds_read_b64_tr_b16 v[194:195], v152 offset:1536
	ds_read_b64_tr_b16 v[196:197], v152 offset:3584
	v_mfma_f32_32x32x16_bf16 v[18:33], v[74:77], v[198:201], v[18:33]
	ds_read_b64_tr_b16 v[198:199], v152 offset:5632
	ds_read_b64_tr_b16 v[200:201], v152 offset:7680
	v_mfma_f32_32x32x16_bf16 v[18:33], v[78:81], v[202:205], v[18:33]
	s_waitcnt lgkmcnt(13)
	ds_read_b64_tr_b16 v[202:203], v152 offset:9728
	ds_read_b64_tr_b16 v[204:205], v152 offset:11776
	v_mfma_f32_32x32x16_bf16 v[34:49], v[66:69], v[206:209], v[2:17]
	s_waitcnt lgkmcnt(13)
	ds_read_b64_tr_b16 v[206:207], v152 offset:13824
	ds_read_b64_tr_b16 v[208:209], v152 offset:15872
	v_mfma_f32_32x32x16_bf16 v[34:49], v[70:73], v[210:213], v[34:49]
	v_mfma_f32_32x32x16_bf16 v[34:49], v[74:77], v[214:217], v[34:49]
	s_waitcnt lgkmcnt(15)
	v_mfma_f32_32x32x16_bf16 v[34:49], v[78:81], v[218:221], v[34:49]
	s_waitcnt lgkmcnt(14)
	v_mfma_f32_32x32x16_bf16 v[50:65], v[66:69], v[222:225], v[2:17]
	s_waitcnt lgkmcnt(12)
	v_mfma_f32_32x32x16_bf16 v[50:65], v[70:73], v[226:229], v[50:65]
	s_waitcnt lgkmcnt(10)
	v_mfma_f32_32x32x16_bf16 v[50:65], v[74:77], v[230:233], v[50:65]
	s_waitcnt lgkmcnt(8)
	v_mfma_f32_32x32x16_bf16 v[50:65], v[78:81], v[190:193], v[50:65]
	s_waitcnt lgkmcnt(6)
	v_mfma_f32_32x32x16_bf16 v[2:17], v[66:69], v[194:197], v[2:17]
	s_cmp_lt_u32 s33, 2
	s_waitcnt lgkmcnt(4)
	v_mfma_f32_32x32x16_bf16 v[2:17], v[70:73], v[198:201], v[2:17]
	s_waitcnt lgkmcnt(2)
	v_mfma_f32_32x32x16_bf16 v[2:17], v[74:77], v[202:205], v[2:17]
	s_waitcnt lgkmcnt(0)
	v_mfma_f32_32x32x16_bf16 v[2:17], v[78:81], v[206:209], v[2:17]
	s_cbranch_scc0 .LBB0_692
	s_cmp_lt_u32 s33, 3
	s_cbranch_scc0 .LBB0_699

; template <int DQK, int KB>
; __device__ __forceinline__ void qkt(f32x16& p0, f32x16& p1, const char* K_lds, int r32, int hi, const bf16x8* qr) {
;     constexpr int ROWB = DQK * 2, SHM_K = 64 * ROWB;
;     p0 = f32x16{}; p1 = f32x16{};
;     const char* kb[4];
; #pragma unroll
;     for (int dd = 0; dd < 4; ++dd) kb[dd] = K_lds + KB * SHM_K + r32 * ROWB + (((dd * 16 + hi * 8) * 2) ^ ((r32 & 7) << 4));
; #pragma unroll
;     for (int d0 = 0; d0 < DQK / 16; ++d0) { const char* a = kb[d0 & 3] + (d0 >> 2) * 128;
;         bf16x8 b0 = *reinterpret_cast<const bf16x8*>(a);
;         bf16x8 b1 = *reinterpret_cast<const bf16x8*>(a + 32 * ROWB);
;         p0 = __builtin_amdgcn_mfma_f32_32x32x16_bf16(b0, qr[d0], p0, 0, 0, 0);
;         p1 = __builtin_amdgcn_mfma_f32_32x32x16_bf16(b1, qr[d0], p1, 0, 0, 0); }
.LBB0_692:
	s_cmp_gt_u32 s80, 3
	ds_read_b128 v[190:193], v166 offset:16384
	ds_read_b128 v[194:197], v166 offset:24576
	ds_read_b128 v[198:201], v167 offset:16384
	ds_read_b128 v[202:205], v167 offset:24576
	ds_read_b128 v[206:209], v168 offset:16384
	ds_read_b128 v[210:213], v168 offset:24576
	ds_read_b128 v[214:217], v169 offset:16384
	ds_read_b128 v[218:221], v169 offset:24576
	ds_read_b128 v[222:225], v166 offset:16512
	ds_read_b128 v[226:229], v166 offset:24704
	ds_read_b128 v[230:233], v167 offset:16512
	ds_read_b128 v[234:237], v167 offset:24704
	ds_read_b128 v[238:241], v168 offset:16512
	s_waitcnt lgkmcnt(12)
	v_mfma_f32_32x32x16_bf16 v[82:97], v[190:193], v[126:129], 0
	ds_read_b128 v[242:245], v168 offset:24704
	s_waitcnt lgkmcnt(12)
	v_mfma_f32_32x32x16_bf16 v[66:81], v[194:197], v[126:129], 0
	ds_read_b128 v[246:249], v169 offset:16512
	s_waitcnt lgkmcnt(12)
	v_mfma_f32_32x32x16_bf16 v[82:97], v[198:201], v[122:125], v[82:97]
	ds_read_b128 v[250:253], v169 offset:24704
	s_waitcnt lgkmcnt(12)
	v_mfma_f32_32x32x16_bf16 v[66:81], v[202:205], v[122:125], v[66:81]
	s_waitcnt lgkmcnt(11)
	v_mfma_f32_32x32x16_bf16 v[82:97], v[206:209], v[118:121], v[82:97]
	s_waitcnt lgkmcnt(10)
	v_mfma_f32_32x32x16_bf16 v[66:81], v[210:213], v[118:121], v[66:81]
	s_waitcnt lgkmcnt(9)
	v_mfma_f32_32x32x16_bf16 v[82:97], v[214:217], v[114:117], v[82:97]
	s_waitcnt lgkmcnt(8)
	v_mfma_f32_32x32x16_bf16 v[66:81], v[218:221], v[114:117], v[66:81]
	s_waitcnt lgkmcnt(7)
	v_mfma_f32_32x32x16_bf16 v[82:97], v[222:225], v[110:113], v[82:97]
	s_waitcnt lgkmcnt(6)
	v_mfma_f32_32x32x16_bf16 v[66:81], v[226:229], v[110:113], v[66:81]
	s_waitcnt lgkmcnt(5)
	v_mfma_f32_32x32x16_bf16 v[82:97], v[230:233], v[106:109], v[82:97]
	s_waitcnt lgkmcnt(4)
	v_mfma_f32_32x32x16_bf16 v[66:81], v[234:237], v[106:109], v[66:81]
	s_waitcnt lgkmcnt(3)
	v_mfma_f32_32x32x16_bf16 v[82:97], v[238:241], v[102:105], v[82:97]
	s_waitcnt lgkmcnt(2)
	v_mfma_f32_32x32x16_bf16 v[66:81], v[242:245], v[102:105], v[66:81]
	s_waitcnt lgkmcnt(1)
	v_mfma_f32_32x32x16_bf16 v[82:97], v[246:249], v[98:101], v[82:97]
	v_mov_b32_e32 v174, v151
	s_nop 0
	v_mul_f32_e32 v176, v174, v157
	v_fma_f32 v182, v174, s34, v176
	v_fma_f32 v183, v174, s35, v176
	v_fma_f32 v184, v174, s2, v176
	v_fma_f32 v185, v174, s3, v176
	v_pk_fma_f32 v[186:187], v[174:175], s[36:37], v[176:177] op_sel_hi:[0,1,0]
	s_waitcnt lgkmcnt(0)
	s_waitcnt lgkmcnt(0)
	v_mfma_f32_32x32x16_bf16 v[66:81], v[250:253], v[98:101], v[66:81]
	v_mov_b32_e32 v181, v174
	v_mul_f32_e32 v178, 0x42000000, v174
	v_fma_f32 v180, 0, v174, v176
	v_fmac_f32_e32 v181, v181, v157
	v_fma_f32 v188, v174, s38, v176
	v_fma_f32 v189, v174, s39, v176
	v_pk_fma_f32 v[190:191], v[174:175], s[40:41], v[176:177] op_sel_hi:[0,1,0]
	v_pk_fma_f32 v[192:193], v[174:175], s[42:43], v[176:177] op_sel_hi:[0,1,0]
	v_pk_fma_f32 v[174:175], v[174:175], s[44:45], v[176:177] op_sel_hi:[0,1,0]
	v_pk_add_f32 v[96:97], v[96:97], v[174:175]
	v_pk_add_f32 v[92:93], v[92:93], v[190:191]
	v_pk_add_f32 v[90:91], v[90:91], v[188:189]
	v_pk_add_f32 v[88:89], v[88:89], v[186:187]
	v_pk_add_f32 v[86:87], v[86:87], v[184:185]
	v_pk_add_f32 v[84:85], v[84:85], v[182:183]
	v_pk_add_f32 v[176:177], v[178:179], v[182:183] op_sel_hi:[0,1]
	v_pk_add_f32 v[182:183], v[178:179], v[184:185] op_sel_hi:[0,1]
	v_pk_add_f32 v[184:185], v[178:179], v[186:187] op_sel_hi:[0,1]
	v_pk_add_f32 v[186:187], v[178:179], v[188:189] op_sel_hi:[0,1]
	v_pk_add_f32 v[188:189], v[178:179], v[190:191] op_sel_hi:[0,1]
	v_pk_add_f32 v[190:191], v[178:179], v[192:193] op_sel_hi:[0,1]
	v_pk_add_f32 v[174:175], v[178:179], v[174:175] op_sel_hi:[0,1]
	v_pk_add_f32 v[178:179], v[178:179], v[180:181] op_sel_hi:[0,1]
	v_pk_add_f32 v[94:95], v[94:95], v[192:193]
	v_pk_add_f32 v[82:83], v[82:83], v[180:181]
	v_pk_add_f32 v[80:81], v[80:81], v[174:175]
	v_pk_add_f32 v[78:79], v[78:79], v[190:191]
	v_pk_add_f32 v[76:77], v[76:77], v[188:189]
	v_pk_add_f32 v[74:75], v[74:75], v[186:187]
	v_pk_add_f32 v[72:73], v[72:73], v[184:185]
	v_pk_add_f32 v[70:71], v[70:71], v[182:183]
	v_pk_add_f32 v[68:69], v[68:69], v[176:177]
	v_pk_add_f32 v[66:67], v[66:67], v[178:179]
	s_cbranch_scc1 .LBB0_694
; __device__ __forceinline__ void mask_tile(f32x16& p0, f32x16& p1, int dq) {
;     const float NEG = -__builtin_inff();
; #pragma unroll
;     for (int r = 0; r < 16; ++r) {
;         const int c = (r & 3) + 8 * (r >> 2);
;         if (dq - c < 0) p0[r] = NEG;
;         if (dq - c - 32 < 0) p1[r] = NEG;
;     }
; }
	v_sub_u32_e32 v171, v132, v154
	v_subrev_u32_e32 v171, 64, v171
	v_cmp_gt_i32_e64 s[66:67], 26, v171
	v_cmp_gt_i32_e64 s[68:69], 27, v171
	v_cmp_gt_i32_e64 s[64:65], 25, v171
	s_and_b64 s[66:67], s[68:69], s[66:67]
	v_cmp_gt_i32_e64 s[62:63], 24, v171
	s_and_b64 s[64:65], s[66:67], s[64:65]
	v_cmp_gt_i32_e64 s[60:61], 19, v171
	s_and_b64 s[62:63], s[64:65], s[62:63]
	v_cmp_gt_i32_e64 s[58:59], 18, v171
	s_and_b64 s[60:61], s[62:63], s[60:61]
	v_cmp_gt_i32_e64 s[56:57], 17, v171
	s_and_b64 s[58:59], s[60:61], s[58:59]
	v_cmp_gt_i32_e64 s[54:55], 16, v171
	s_and_b64 s[56:57], s[58:59], s[56:57]
	v_cmp_gt_i32_e64 s[52:53], 11, v171
	s_and_b64 s[54:55], s[56:57], s[54:55]
	v_cmp_gt_i32_e64 s[50:51], 10, v171
	s_and_b64 s[52:53], s[54:55], s[52:53]
	v_cmp_gt_i32_e64 s[48:49], 9, v171
	s_and_b64 s[50:51], s[52:53], s[50:51]
	v_cmp_gt_i32_e64 s[46:47], 8, v171
	s_and_b64 s[48:49], s[50:51], s[48:49]
	v_cmp_gt_i32_e64 s[44:45], 3, v171
	s_and_b64 s[46:47], s[48:49], s[46:47]
	v_cmp_gt_i32_e64 s[42:43], 2, v171
	s_and_b64 s[44:45], s[46:47], s[44:45]
	v_cmp_gt_i32_e64 s[40:41], 1, v171
	s_and_b64 s[42:43], s[44:45], s[42:43]
	v_cmp_gt_i32_e64 s[38:39], 0, v171
	s_and_b64 s[40:41], s[42:43], s[40:41]
	s_and_b64 s[38:39], s[40:41], s[38:39]
	v_cmp_gt_i32_e64 s[36:37], 58, v171
	v_cndmask_b32_e64 v82, v82, v147, s[38:39]
	v_cmp_gt_i32_e64 s[38:39], 59, v171
	v_cmp_gt_i32_e64 s[34:35], 57, v171
	s_and_b64 s[36:37], s[38:39], s[36:37]
	v_cmp_gt_i32_e64 s[30:31], 56, v171
	s_and_b64 s[34:35], s[36:37], s[34:35]
	v_cmp_gt_i32_e64 s[28:29], 51, v171
	s_and_b64 s[30:31], s[34:35], s[30:31]
	v_cmp_gt_i32_e64 s[26:27], 50, v171
	s_and_b64 s[28:29], s[30:31], s[28:29]
	v_cmp_gt_i32_e64 s[24:25], 49, v171
	s_and_b64 s[26:27], s[28:29], s[26:27]
	v_cmp_gt_i32_e64 s[22:23], 48, v171
	s_and_b64 s[24:25], s[26:27], s[24:25]
	v_cmp_gt_i32_e64 s[20:21], 43, v171
	s_and_b64 s[22:23], s[24:25], s[22:23]
	v_cmp_gt_i32_e64 s[18:19], 42, v171
	s_and_b64 s[20:21], s[22:23], s[20:21]
	v_cmp_gt_i32_e64 s[16:17], 41, v171
	s_and_b64 s[18:19], s[20:21], s[18:19]
	v_cmp_gt_i32_e64 s[14:15], 40, v171
	s_and_b64 s[16:17], s[18:19], s[16:17]
	v_cmp_gt_i32_e64 s[12:13], 35, v171
	s_and_b64 s[14:15], s[16:17], s[14:15]
	v_cmp_gt_i32_e64 s[10:11], 34, v171
	s_and_b64 s[12:13], s[14:15], s[12:13]
	v_cmp_gt_i32_e64 s[8:9], 33, v171
	s_and_b64 s[10:11], s[12:13], s[10:11]
	v_cmp_gt_i32_e32 vcc, 32, v171
	s_and_b64 s[8:9], s[10:11], s[8:9]
	v_cndmask_b32_e64 v85, v85, v147, s[44:45]
	s_mov_b32 s44, 0x41d00000
	v_cndmask_b32_e64 v84, v84, v147, s[42:43]
	s_mov_b32 s42, 0x41c00000
	v_cndmask_b32_e64 v83, v83, v147, s[40:41]
	s_mov_b32 s40, 0x41900000
	v_cndmask_b32_e64 v81, v81, v147, s[38:39]
	s_mov_b32 s38, 0x41800000
	v_cndmask_b32_e64 v80, v80, v147, s[36:37]
	s_mov_b32 s36, 0x41200000
	v_cndmask_b32_e64 v79, v79, v147, s[34:35]
	s_mov_b32 s34, 2.0
	s_and_b64 vcc, s[8:9], vcc
	v_cndmask_b32_e64 v97, v97, v147, s[68:69]
	v_cndmask_b32_e64 v96, v96, v147, s[66:67]
	v_cndmask_b32_e64 v95, v95, v147, s[64:65]
	v_cndmask_b32_e64 v94, v94, v147, s[62:63]
	v_cndmask_b32_e64 v93, v93, v147, s[60:61]
	v_cndmask_b32_e64 v92, v92, v147, s[58:59]
	v_cndmask_b32_e64 v91, v91, v147, s[56:57]
	v_cndmask_b32_e64 v90, v90, v147, s[54:55]
	v_cndmask_b32_e64 v89, v89, v147, s[52:53]
	v_cndmask_b32_e64 v88, v88, v147, s[50:51]
	v_cndmask_b32_e64 v87, v87, v147, s[48:49]
	v_cndmask_b32_e64 v86, v86, v147, s[46:47]
	s_mov_b32 s45, 0x41d80000
	s_mov_b32 s43, 0x41c80000
	s_mov_b32 s41, 0x41980000
	s_mov_b32 s39, 0x41880000
	s_mov_b32 s37, 0x41300000
	s_mov_b32 s35, 0x40400000
	v_cndmask_b32_e64 v78, v78, v147, s[30:31]
	v_cndmask_b32_e64 v77, v77, v147, s[28:29]
	v_cndmask_b32_e64 v76, v76, v147, s[26:27]
	v_cndmask_b32_e64 v75, v75, v147, s[24:25]
	v_cndmask_b32_e64 v74, v74, v147, s[22:23]
	v_cndmask_b32_e64 v73, v73, v147, s[20:21]
	v_cndmask_b32_e64 v72, v72, v147, s[18:19]
	v_cndmask_b32_e64 v71, v71, v147, s[16:17]
	v_cndmask_b32_e64 v70, v70, v147, s[14:15]
	v_cndmask_b32_e64 v69, v69, v147, s[12:13]
	v_cndmask_b32_e64 v68, v68, v147, s[10:11]
	v_cndmask_b32_e64 v67, v67, v147, s[8:9]
	v_cndmask_b32_e32 v66, v66, v147, vcc

; template <int DQK> __device__ __forceinline__ void partialSM(f32x16& p0, f32x16& p1, float& m_reg, float& mn, float& alpha) {
;     ...
;     for (int r = 0; r < 16; ++r) p0[r] = fmaf(p0[r], C2, mnL);
; #pragma unroll
;     for (int r = 0; r < 16; ++r) p1[r] = fmaf(p1[r], C2, mnL);
; #pragma unroll
;     for (int r = 0; r < 16; ++r) p0[r] = __builtin_amdgcn_exp2f(p0[r]);
; }
; __device__ __forceinline__ void finishSM(f32x16& p0, f32x16& p1, float alpha, float& l_reg, bf16x8& pa0, bf16x8& pa1, bf16x8& pa2, bf16x8& pa3) {
; #pragma unroll
;     for (int r = 0; r < 16; ++r) p1[r] = __builtin_amdgcn_exp2f(p1[r]);
;     float ps = 0;
; #pragma unroll
;     for (int r = 0; r < 16; ++r) ps += p0[r];
; #pragma unroll
;     for (int r = 0; r < 16; ++r) ps += p1[r];
;     { auto rr = __builtin_amdgcn_permlane32_swap(__float_as_uint(ps), __float_as_uint(ps), false, false);
;       ps = __uint_as_float(rr[0]) + __uint_as_float(rr[1]); }
;     l_reg = l_reg * alpha + ps;
;     ...
;     PK4(p0, 0, pa0); PK4(p0, 8, pa1); PK4(p1, 0, pa2); PK4(p1, 8, pa3);
;     ...
; }
; template <int VB>
; __device__ __forceinline__ void pv_tile(f32x16* o, int vb0, bf16x8 pa0, bf16x8 pa1, bf16x8 pa2, bf16x8 pa3) {
;     ...
;     PV_D0(0); PV_D0(1); PV_D0(2); PV_D0(3);
.LBB0_698:
	ds_read_b64_tr_b16 v[190:191], v152 offset:16384
	ds_read_b64_tr_b16 v[192:193], v152 offset:18432
	ds_read_b64_tr_b16 v[194:195], v152 offset:20480
	ds_read_b64_tr_b16 v[196:197], v152 offset:22528
	ds_read_b64_tr_b16 v[198:199], v152 offset:24576
	ds_read_b64_tr_b16 v[200:201], v152 offset:26624
	ds_read_b64_tr_b16 v[202:203], v152 offset:28672
	ds_read_b64_tr_b16 v[204:205], v152 offset:30720
	ds_read_b64_tr_b16 v[206:207], v152 offset:16896
	ds_read_b64_tr_b16 v[208:209], v152 offset:18944
	ds_read_b64_tr_b16 v[210:211], v152 offset:20992
	ds_read_b64_tr_b16 v[212:213], v152 offset:23040
	ds_read_b64_tr_b16 v[214:215], v152 offset:25088
	ds_read_b64_tr_b16 v[216:217], v152 offset:27136
	v_cndmask_b32_e64 v137, v137, v173, s[8:9]
	v_mul_f32_e32 v173, 0xbe0293ee, v137
	v_fmamk_f32 v82, v82, 0x3e0293ee, v173
	v_fmamk_f32 v83, v83, 0x3e0293ee, v173
	v_fmamk_f32 v84, v84, 0x3e0293ee, v173
	v_fmamk_f32 v85, v85, 0x3e0293ee, v173
	v_fmamk_f32 v86, v86, 0x3e0293ee, v173
	v_fmamk_f32 v87, v87, 0x3e0293ee, v173
	v_fmamk_f32 v88, v88, 0x3e0293ee, v173
	v_fmamk_f32 v89, v89, 0x3e0293ee, v173
	v_fmamk_f32 v90, v90, 0x3e0293ee, v173
	v_fmamk_f32 v91, v91, 0x3e0293ee, v173
	v_fmamk_f32 v92, v92, 0x3e0293ee, v173
	v_fmamk_f32 v93, v93, 0x3e0293ee, v173
	v_fmamk_f32 v94, v94, 0x3e0293ee, v173
	v_fmamk_f32 v95, v95, 0x3e0293ee, v173
	v_fmamk_f32 v96, v96, 0x3e0293ee, v173
	v_fmamk_f32 v97, v97, 0x3e0293ee, v173
	v_fmamk_f32 v66, v66, 0x3e0293ee, v173
	v_fmamk_f32 v67, v67, 0x3e0293ee, v173
	v_fmamk_f32 v68, v68, 0x3e0293ee, v173
	v_fmamk_f32 v69, v69, 0x3e0293ee, v173
	v_fmamk_f32 v70, v70, 0x3e0293ee, v173
	v_fmamk_f32 v71, v71, 0x3e0293ee, v173
	v_fmamk_f32 v72, v72, 0x3e0293ee, v173
	v_fmamk_f32 v73, v73, 0x3e0293ee, v173
	v_fmamk_f32 v74, v74, 0x3e0293ee, v173
	v_fmamk_f32 v75, v75, 0x3e0293ee, v173
	v_fmamk_f32 v76, v76, 0x3e0293ee, v173
	v_fmamk_f32 v77, v77, 0x3e0293ee, v173
	v_fmamk_f32 v78, v78, 0x3e0293ee, v173
	v_fmamk_f32 v79, v79, 0x3e0293ee, v173
	v_fmamk_f32 v80, v80, 0x3e0293ee, v173
	v_fmac_f32_e32 v173, 0x3e0293ee, v81
	v_exp_f32_e32 v81, v82
	v_exp_f32_e32 v82, v83
	v_exp_f32_e32 v83, v84
	v_exp_f32_e32 v84, v85
	v_exp_f32_e32 v85, v86
	v_exp_f32_e32 v86, v87
	v_exp_f32_e32 v87, v88
	v_exp_f32_e32 v88, v89
	v_exp_f32_e32 v89, v90
	v_exp_f32_e32 v90, v91
	v_exp_f32_e32 v91, v92
	v_exp_f32_e32 v92, v93
	v_exp_f32_e32 v93, v94
	v_exp_f32_e32 v94, v95
	v_exp_f32_e32 v95, v96
	v_exp_f32_e32 v96, v97
	v_exp_f32_e32 v97, v66
	v_add_f32_e32 v66, 0, v81
	v_add_f32_e32 v66, v82, v66
	v_add_f32_e32 v66, v83, v66
	v_add_f32_e32 v66, v84, v66
	v_add_f32_e32 v66, v85, v66
	v_add_f32_e32 v66, v86, v66
	v_add_f32_e32 v66, v87, v66
	v_add_f32_e32 v66, v88, v66
	v_add_f32_e32 v66, v89, v66
	v_add_f32_e32 v66, v90, v66
	v_add_f32_e32 v66, v91, v66
	v_add_f32_e32 v66, v92, v66
	v_add_f32_e32 v66, v93, v66
	v_exp_f32_e32 v174, v67
	v_add_f32_e32 v66, v94, v66
	v_exp_f32_e32 v175, v68
	v_add_f32_e32 v66, v95, v66
	v_exp_f32_e32 v176, v69
	v_add_f32_e32 v66, v96, v66
	v_exp_f32_e32 v177, v70
	v_add_f32_e32 v66, v97, v66
	v_exp_f32_e32 v178, v71
	v_add_f32_e32 v66, v174, v66
	v_exp_f32_e32 v179, v72
	v_add_f32_e32 v66, v175, v66
	v_exp_f32_e32 v180, v73
	v_add_f32_e32 v66, v176, v66
	v_exp_f32_e32 v181, v74
	v_add_f32_e32 v66, v177, v66
	v_exp_f32_e32 v182, v75
	v_add_f32_e32 v66, v178, v66
	v_exp_f32_e32 v183, v76
	v_add_f32_e32 v66, v179, v66
	v_exp_f32_e32 v184, v77
	v_add_f32_e32 v66, v180, v66
	v_exp_f32_e32 v185, v78
	v_add_f32_e32 v66, v181, v66
	v_exp_f32_e32 v186, v79
	v_add_f32_e32 v66, v182, v66
	v_exp_f32_e32 v187, v80
	v_add_f32_e32 v66, v183, v66
	v_exp_f32_e32 v173, v173
	v_add_f32_e32 v66, v184, v66
	v_add_f32_e32 v66, v185, v66
	v_add_f32_e32 v66, v186, v66
	v_add_f32_e32 v66, v187, v66
	v_add_f32_e32 v66, v173, v66
	v_mov_b32_e32 v67, v66
	s_nop 1
	v_permlane32_swap_b32_e32 v66, v67
	v_add_f32_e32 v188, v66, v67
	v_cvt_pk_bf16_f32 v66, v81, v82
	v_cvt_pk_bf16_f32 v67, v83, v84
	v_cvt_pk_bf16_f32 v68, v85, v86
	v_cvt_pk_bf16_f32 v69, v87, v88
	v_cvt_pk_bf16_f32 v70, v89, v90
	v_cvt_pk_bf16_f32 v71, v91, v92
	v_cvt_pk_bf16_f32 v72, v93, v94
	v_cvt_pk_bf16_f32 v73, v95, v96
	v_cvt_pk_bf16_f32 v74, v97, v174
	v_cvt_pk_bf16_f32 v75, v175, v176
	v_cvt_pk_bf16_f32 v76, v177, v178
	v_cvt_pk_bf16_f32 v77, v179, v180
	v_cvt_pk_bf16_f32 v78, v181, v182
	v_cvt_pk_bf16_f32 v79, v183, v184
	v_cvt_pk_bf16_f32 v80, v185, v186
	v_cvt_pk_bf16_f32 v81, v187, v173
	v_fmac_f32_e32 v188, v145, v171
	v_permlane32_swap_b32_e32 v66, v68
	v_permlane32_swap_b32_e32 v67, v69
	v_permlane32_swap_b32_e32 v70, v72
	v_permlane32_swap_b32_e32 v71, v73
	v_permlane32_swap_b32_e32 v74, v76
	v_permlane32_swap_b32_e32 v75, v77
	v_permlane32_swap_b32_e32 v78, v80
	v_permlane32_swap_b32_e32 v79, v81
	s_waitcnt lgkmcnt(0)
	ds_read_b64_tr_b16 v[218:219], v152 offset:29184
	ds_read_b64_tr_b16 v[220:221], v152 offset:31232
	ds_read_b64_tr_b16 v[222:223], v152 offset:17408
	ds_read_b64_tr_b16 v[224:225], v152 offset:19456
	ds_read_b64_tr_b16 v[226:227], v152 offset:21504
	ds_read_b64_tr_b16 v[228:229], v152 offset:23552
	ds_read_b64_tr_b16 v[230:231], v152 offset:25600
	ds_read_b64_tr_b16 v[232:233], v152 offset:27648
	v_mfma_f32_32x32x16_bf16 v[18:33], v[66:69], v[190:193], v[18:33]
	ds_read_b64_tr_b16 v[190:191], v152 offset:29696
	ds_read_b64_tr_b16 v[192:193], v152 offset:31744
	v_mfma_f32_32x32x16_bf16 v[18:33], v[70:73], v[194:197], v[18:33]
	ds_read_b64_tr_b16 v[194:195], v152 offset:17920
	ds_read_b64_tr_b16 v[196:197], v152 offset:19968
	v_mfma_f32_32x32x16_bf16 v[18:33], v[74:77], v[198:201], v[18:33]
	ds_read_b64_tr_b16 v[198:199], v152 offset:22016
	ds_read_b64_tr_b16 v[200:201], v152 offset:24064
	v_mfma_f32_32x32x16_bf16 v[18:33], v[78:81], v[202:205], v[18:33]
	s_waitcnt lgkmcnt(13)
; template <int DQK, int KB>
; __device__ __forceinline__ void qkt(f32x16& p0, f32x16& p1, const char* K_lds, int r32, int hi, const bf16x8* qr) {
;     constexpr int ROWB = DQK * 2, SHM_K = 64 * ROWB;
;     p0 = f32x16{}; p1 = f32x16{};
;     const char* kb[4];
; #pragma unroll
;     for (int dd = 0; dd < 4; ++dd) kb[dd] = K_lds + KB * SHM_K + r32 * ROWB + (((dd * 16 + hi * 8) * 2) ^ ((r32 & 7) << 4));
; #pragma unroll
;     for (int d0 = 0; d0 < DQK / 16; ++d0) { const char* a = kb[d0 & 3] + (d0 >> 2) * 128;
;         bf16x8 b0 = *reinterpret_cast<const bf16x8*>(a);
;         bf16x8 b1 = *reinterpret_cast<const bf16x8*>(a + 32 * ROWB);
;         p0 = __builtin_amdgcn_mfma_f32_32x32x16_bf16(b0, qr[d0], p0, 0, 0, 0);
;         p1 = __builtin_amdgcn_mfma_f32_32x32x16_bf16(b1, qr[d0], p1, 0, 0, 0); }
; template <int VB>
; __device__ __forceinline__ void pv_tile(f32x16* o, int vb0, bf16x8 pa0, bf16x8 pa1, bf16x8 pa2, bf16x8 pa3) {
;     ...
;     PV_D0(0); PV_D0(1); PV_D0(2); PV_D0(3);
	ds_read_b64_tr_b16 v[202:203], v152 offset:26112
	ds_read_b64_tr_b16 v[204:205], v152 offset:28160
	v_mfma_f32_32x32x16_bf16 v[34:49], v[66:69], v[206:209], v[34:49]
	s_waitcnt lgkmcnt(13)
	ds_read_b64_tr_b16 v[206:207], v152 offset:30208
	ds_read_b64_tr_b16 v[208:209], v152 offset:32256
	v_mfma_f32_32x32x16_bf16 v[34:49], v[70:73], v[210:213], v[34:49]
	v_mfma_f32_32x32x16_bf16 v[34:49], v[74:77], v[214:217], v[34:49]
	s_waitcnt lgkmcnt(15)
	v_mfma_f32_32x32x16_bf16 v[34:49], v[78:81], v[218:221], v[34:49]
	s_waitcnt lgkmcnt(14)
	v_mfma_f32_32x32x16_bf16 v[50:65], v[66:69], v[222:225], v[50:65]
	s_waitcnt lgkmcnt(12)
	v_mfma_f32_32x32x16_bf16 v[50:65], v[70:73], v[226:229], v[50:65]
	s_waitcnt lgkmcnt(10)
	v_mfma_f32_32x32x16_bf16 v[50:65], v[74:77], v[230:233], v[50:65]
	s_waitcnt lgkmcnt(8)
	v_mfma_f32_32x32x16_bf16 v[50:65], v[78:81], v[190:193], v[50:65]
	s_waitcnt lgkmcnt(6)
	v_mfma_f32_32x32x16_bf16 v[2:17], v[66:69], v[194:197], v[2:17]
	v_mov_b32_e32 v145, v188
	s_waitcnt lgkmcnt(4)
	v_mfma_f32_32x32x16_bf16 v[2:17], v[70:73], v[198:201], v[2:17]
	s_waitcnt lgkmcnt(2)
	v_mfma_f32_32x32x16_bf16 v[2:17], v[74:77], v[202:205], v[2:17]
	s_waitcnt lgkmcnt(0)
	v_mfma_f32_32x32x16_bf16 v[2:17], v[78:81], v[206:209], v[2:17]
	s_cmp_lt_u32 s33, 3
	s_cbranch_scc1 .LBB0_561
.LBB0_699:
	s_cmp_gt_u32 s80, 5
	ds_read_b128 v[190:193], v166 offset:32768
	ds_read_b128 v[194:197], v166 offset:40960
	ds_read_b128 v[198:201], v167 offset:32768
	ds_read_b128 v[202:205], v167 offset:40960
	ds_read_b128 v[206:209], v168 offset:32768
	ds_read_b128 v[210:213], v168 offset:40960
	ds_read_b128 v[214:217], v169 offset:32768
	ds_read_b128 v[218:221], v169 offset:40960
	ds_read_b128 v[222:225], v166 offset:32896
	ds_read_b128 v[226:229], v166 offset:41088
	ds_read_b128 v[230:233], v167 offset:32896
	ds_read_b128 v[234:237], v167 offset:41088
	ds_read_b128 v[238:241], v168 offset:32896
	s_waitcnt lgkmcnt(12)
	v_mfma_f32_32x32x16_bf16 v[82:97], v[190:193], v[126:129], 0
	ds_read_b128 v[242:245], v168 offset:41088
	s_waitcnt lgkmcnt(12)
	v_mfma_f32_32x32x16_bf16 v[66:81], v[194:197], v[126:129], 0
	ds_read_b128 v[246:249], v169 offset:32896
	s_waitcnt lgkmcnt(12)
	v_mfma_f32_32x32x16_bf16 v[82:97], v[198:201], v[122:125], v[82:97]
	ds_read_b128 v[250:253], v169 offset:41088
	s_waitcnt lgkmcnt(12)
	v_mfma_f32_32x32x16_bf16 v[66:81], v[202:205], v[122:125], v[66:81]
	s_waitcnt lgkmcnt(11)
	v_mfma_f32_32x32x16_bf16 v[82:97], v[206:209], v[118:121], v[82:97]
	s_waitcnt lgkmcnt(10)
	v_mfma_f32_32x32x16_bf16 v[66:81], v[210:213], v[118:121], v[66:81]
	s_waitcnt lgkmcnt(9)
	v_mfma_f32_32x32x16_bf16 v[82:97], v[214:217], v[114:117], v[82:97]
	s_waitcnt lgkmcnt(8)
	v_mfma_f32_32x32x16_bf16 v[66:81], v[218:221], v[114:117], v[66:81]
	s_waitcnt lgkmcnt(7)
	v_mfma_f32_32x32x16_bf16 v[82:97], v[222:225], v[110:113], v[82:97]
	s_waitcnt lgkmcnt(6)
	v_mfma_f32_32x32x16_bf16 v[66:81], v[226:229], v[110:113], v[66:81]
	s_waitcnt lgkmcnt(5)
	v_mfma_f32_32x32x16_bf16 v[82:97], v[230:233], v[106:109], v[82:97]
	s_waitcnt lgkmcnt(4)
	v_mfma_f32_32x32x16_bf16 v[66:81], v[234:237], v[106:109], v[66:81]
	s_waitcnt lgkmcnt(3)
	v_mfma_f32_32x32x16_bf16 v[82:97], v[238:241], v[102:105], v[82:97]
	s_waitcnt lgkmcnt(2)
	v_mfma_f32_32x32x16_bf16 v[66:81], v[242:245], v[102:105], v[66:81]
	s_waitcnt lgkmcnt(1)
	v_mfma_f32_32x32x16_bf16 v[82:97], v[246:249], v[98:101], v[82:97]
	v_mov_b32_e32 v174, v151
	s_nop 0
	v_mul_f32_e32 v176, v174, v158
	v_fma_f32 v182, v174, s34, v176
	v_fma_f32 v183, v174, s35, v176
	v_fma_f32 v184, v174, s2, v176
	v_fma_f32 v185, v174, s3, v176
	v_pk_fma_f32 v[186:187], v[174:175], s[36:37], v[176:177] op_sel_hi:[0,1,0]
	s_waitcnt lgkmcnt(0)
	s_waitcnt lgkmcnt(0)
	v_mfma_f32_32x32x16_bf16 v[66:81], v[250:253], v[98:101], v[66:81]
	v_mov_b32_e32 v181, v174
	v_mul_f32_e32 v178, 0x42000000, v174
	v_fma_f32 v180, 0, v174, v176
	v_fmac_f32_e32 v181, v181, v158
	v_fma_f32 v188, v174, s38, v176
	v_fma_f32 v189, v174, s39, v176
	v_pk_fma_f32 v[190:191], v[174:175], s[40:41], v[176:177] op_sel_hi:[0,1,0]
	v_pk_fma_f32 v[192:193], v[174:175], s[42:43], v[176:177] op_sel_hi:[0,1,0]
	v_pk_fma_f32 v[174:175], v[174:175], s[44:45], v[176:177] op_sel_hi:[0,1,0]
	v_pk_add_f32 v[96:97], v[96:97], v[174:175]
	v_pk_add_f32 v[92:93], v[92:93], v[190:191]
	v_pk_add_f32 v[90:91], v[90:91], v[188:189]
	v_pk_add_f32 v[88:89], v[88:89], v[186:187]
	v_pk_add_f32 v[86:87], v[86:87], v[184:185]
	v_pk_add_f32 v[84:85], v[84:85], v[182:183]
	v_pk_add_f32 v[176:177], v[178:179], v[182:183] op_sel_hi:[0,1]
	v_pk_add_f32 v[182:183], v[178:179], v[184:185] op_sel_hi:[0,1]
	v_pk_add_f32 v[184:185], v[178:179], v[186:187] op_sel_hi:[0,1]
	v_pk_add_f32 v[186:187], v[178:179], v[188:189] op_sel_hi:[0,1]
	v_pk_add_f32 v[188:189], v[178:179], v[190:191] op_sel_hi:[0,1]
	v_pk_add_f32 v[190:191], v[178:179], v[192:193] op_sel_hi:[0,1]
	v_pk_add_f32 v[174:175], v[178:179], v[174:175] op_sel_hi:[0,1]
	v_pk_add_f32 v[178:179], v[178:179], v[180:181] op_sel_hi:[0,1]
	v_pk_add_f32 v[94:95], v[94:95], v[192:193]
	v_pk_add_f32 v[82:83], v[82:83], v[180:181]
	v_pk_add_f32 v[80:81], v[80:81], v[174:175]
	v_pk_add_f32 v[78:79], v[78:79], v[190:191]
	v_pk_add_f32 v[76:77], v[76:77], v[188:189]
	v_pk_add_f32 v[74:75], v[74:75], v[186:187]
	v_pk_add_f32 v[72:73], v[72:73], v[184:185]
	v_pk_add_f32 v[70:71], v[70:71], v[182:183]
	v_pk_add_f32 v[68:69], v[68:69], v[176:177]
	v_pk_add_f32 v[66:67], v[66:67], v[178:179]
	s_cbranch_scc1 .LBB0_701
; __device__ __forceinline__ void mask_tile(f32x16& p0, f32x16& p1, int dq) {
;     const float NEG = -__builtin_inff();
; #pragma unroll
;     for (int r = 0; r < 16; ++r) {
;         const int c = (r & 3) + 8 * (r >> 2);
;         if (dq - c < 0) p0[r] = NEG;
;         if (dq - c - 32 < 0) p1[r] = NEG;
;     }
; }
	v_sub_u32_e32 v171, v132, v154
	v_add_u32_e32 v171, 0xffffff80, v171
	v_cmp_gt_i32_e64 s[66:67], 26, v171
	v_cmp_gt_i32_e64 s[68:69], 27, v171
	v_cmp_gt_i32_e64 s[64:65], 25, v171
	s_and_b64 s[66:67], s[68:69], s[66:67]
	v_cmp_gt_i32_e64 s[62:63], 24, v171
	s_and_b64 s[64:65], s[66:67], s[64:65]
	v_cmp_gt_i32_e64 s[60:61], 19, v171
	s_and_b64 s[62:63], s[64:65], s[62:63]
	v_cmp_gt_i32_e64 s[58:59], 18, v171
	s_and_b64 s[60:61], s[62:63], s[60:61]
	v_cmp_gt_i32_e64 s[56:57], 17, v171
	s_and_b64 s[58:59], s[60:61], s[58:59]
	v_cmp_gt_i32_e64 s[54:55], 16, v171
	s_and_b64 s[56:57], s[58:59], s[56:57]
	v_cmp_gt_i32_e64 s[52:53], 11, v171
	s_and_b64 s[54:55], s[56:57], s[54:55]
	v_cmp_gt_i32_e64 s[50:51], 10, v171
	s_and_b64 s[52:53], s[54:55], s[52:53]
	v_cmp_gt_i32_e64 s[48:49], 9, v171
	s_and_b64 s[50:51], s[52:53], s[50:51]
	v_cmp_gt_i32_e64 s[46:47], 8, v171
	s_and_b64 s[48:49], s[50:51], s[48:49]
	v_cmp_gt_i32_e64 s[44:45], 3, v171
	s_and_b64 s[46:47], s[48:49], s[46:47]
	v_cmp_gt_i32_e64 s[42:43], 2, v171
	s_and_b64 s[44:45], s[46:47], s[44:45]
	v_cmp_gt_i32_e64 s[40:41], 1, v171
	s_and_b64 s[42:43], s[44:45], s[42:43]
	v_cmp_gt_i32_e64 s[38:39], 0, v171
	s_and_b64 s[40:41], s[42:43], s[40:41]
	s_and_b64 s[38:39], s[40:41], s[38:39]
	v_cmp_gt_i32_e64 s[36:37], 58, v171
	v_cndmask_b32_e64 v82, v82, v147, s[38:39]
	v_cmp_gt_i32_e64 s[38:39], 59, v171
	v_cmp_gt_i32_e64 s[34:35], 57, v171
	s_and_b64 s[36:37], s[38:39], s[36:37]
	v_cmp_gt_i32_e64 s[30:31], 56, v171
	s_and_b64 s[34:35], s[36:37], s[34:35]
	v_cmp_gt_i32_e64 s[28:29], 51, v171
	s_and_b64 s[30:31], s[34:35], s[30:31]
	v_cmp_gt_i32_e64 s[26:27], 50, v171
	s_and_b64 s[28:29], s[30:31], s[28:29]
	v_cmp_gt_i32_e64 s[24:25], 49, v171
	s_and_b64 s[26:27], s[28:29], s[26:27]
	v_cmp_gt_i32_e64 s[22:23], 48, v171
	s_and_b64 s[24:25], s[26:27], s[24:25]
	v_cmp_gt_i32_e64 s[20:21], 43, v171
	s_and_b64 s[22:23], s[24:25], s[22:23]
	v_cmp_gt_i32_e64 s[18:19], 42, v171
	s_and_b64 s[20:21], s[22:23], s[20:21]
	v_cmp_gt_i32_e64 s[16:17], 41, v171
	s_and_b64 s[18:19], s[20:21], s[18:19]
	v_cmp_gt_i32_e64 s[14:15], 40, v171
	s_and_b64 s[16:17], s[18:19], s[16:17]
	v_cmp_gt_i32_e64 s[12:13], 35, v171
	s_and_b64 s[14:15], s[16:17], s[14:15]
	v_cmp_gt_i32_e64 s[10:11], 34, v171
	s_and_b64 s[12:13], s[14:15], s[12:13]
	v_cmp_gt_i32_e64 s[8:9], 33, v171
	s_and_b64 s[10:11], s[12:13], s[10:11]
	v_cmp_gt_i32_e32 vcc, 32, v171
	s_and_b64 s[8:9], s[10:11], s[8:9]
	v_cndmask_b32_e64 v85, v85, v147, s[44:45]
	s_mov_b32 s44, 0x41d00000
	v_cndmask_b32_e64 v84, v84, v147, s[42:43]
	s_mov_b32 s42, 0x41c00000
	v_cndmask_b32_e64 v83, v83, v147, s[40:41]
	s_mov_b32 s40, 0x41900000
	v_cndmask_b32_e64 v81, v81, v147, s[38:39]
	s_mov_b32 s38, 0x41800000
	v_cndmask_b32_e64 v80, v80, v147, s[36:37]
	s_mov_b32 s36, 0x41200000
	v_cndmask_b32_e64 v79, v79, v147, s[34:35]
	s_mov_b32 s34, 2.0
	s_and_b64 vcc, s[8:9], vcc
	v_cndmask_b32_e64 v97, v97, v147, s[68:69]
	v_cndmask_b32_e64 v96, v96, v147, s[66:67]
	v_cndmask_b32_e64 v95, v95, v147, s[64:65]
	v_cndmask_b32_e64 v94, v94, v147, s[62:63]
	v_cndmask_b32_e64 v93, v93, v147, s[60:61]
	v_cndmask_b32_e64 v92, v92, v147, s[58:59]
	v_cndmask_b32_e64 v91, v91, v147, s[56:57]
	v_cndmask_b32_e64 v90, v90, v147, s[54:55]
	v_cndmask_b32_e64 v89, v89, v147, s[52:53]
	v_cndmask_b32_e64 v88, v88, v147, s[50:51]
	v_cndmask_b32_e64 v87, v87, v147, s[48:49]
	v_cndmask_b32_e64 v86, v86, v147, s[46:47]
	s_mov_b32 s45, 0x41d80000
	s_mov_b32 s43, 0x41c80000
	s_mov_b32 s41, 0x41980000
	s_mov_b32 s39, 0x41880000
	s_mov_b32 s37, 0x41300000
	s_mov_b32 s35, 0x40400000
	v_cndmask_b32_e64 v78, v78, v147, s[30:31]
	v_cndmask_b32_e64 v77, v77, v147, s[28:29]
	v_cndmask_b32_e64 v76, v76, v147, s[26:27]
	v_cndmask_b32_e64 v75, v75, v147, s[24:25]
	v_cndmask_b32_e64 v74, v74, v147, s[22:23]
	v_cndmask_b32_e64 v73, v73, v147, s[20:21]
	v_cndmask_b32_e64 v72, v72, v147, s[18:19]
	v_cndmask_b32_e64 v71, v71, v147, s[16:17]
	v_cndmask_b32_e64 v70, v70, v147, s[14:15]
	v_cndmask_b32_e64 v69, v69, v147, s[12:13]
	v_cndmask_b32_e64 v68, v68, v147, s[10:11]
	v_cndmask_b32_e64 v67, v67, v147, s[8:9]
	v_cndmask_b32_e32 v66, v66, v147, vcc

; template <int DQK> __device__ __forceinline__ void partialSM(f32x16& p0, f32x16& p1, float& m_reg, float& mn, float& alpha) {
;     ...
;     for (int r = 0; r < 16; ++r) p0[r] = fmaf(p0[r], C2, mnL);
; #pragma unroll
;     for (int r = 0; r < 16; ++r) p1[r] = fmaf(p1[r], C2, mnL);
; #pragma unroll
;     for (int r = 0; r < 16; ++r) p0[r] = __builtin_amdgcn_exp2f(p0[r]);
; }
; __device__ __forceinline__ void finishSM(f32x16& p0, f32x16& p1, float alpha, float& l_reg, bf16x8& pa0, bf16x8& pa1, bf16x8& pa2, bf16x8& pa3) {
; #pragma unroll
;     for (int r = 0; r < 16; ++r) p1[r] = __builtin_amdgcn_exp2f(p1[r]);
;     float ps = 0;
; #pragma unroll
;     for (int r = 0; r < 16; ++r) ps += p0[r];
; #pragma unroll
;     for (int r = 0; r < 16; ++r) ps += p1[r];
;     { auto rr = __builtin_amdgcn_permlane32_swap(__float_as_uint(ps), __float_as_uint(ps), false, false);
;       ps = __uint_as_float(rr[0]) + __uint_as_float(rr[1]); }
;     l_reg = l_reg * alpha + ps;
;     ...
;     PK4(p0, 0, pa0); PK4(p0, 8, pa1); PK4(p1, 0, pa2); PK4(p1, 8, pa3);
;     ...
; }
; template <int VB>
; __device__ __forceinline__ void pv_tile(f32x16* o, int vb0, bf16x8 pa0, bf16x8 pa1, bf16x8 pa2, bf16x8 pa3) {
;     ...
;     PV_D0(0); PV_D0(1); PV_D0(2); PV_D0(3);
.LBB0_705:
	ds_read_b64_tr_b16 v[190:191], v152 offset:32768
	ds_read_b64_tr_b16 v[192:193], v152 offset:34816
	ds_read_b64_tr_b16 v[194:195], v152 offset:36864
	ds_read_b64_tr_b16 v[196:197], v152 offset:38912
	ds_read_b64_tr_b16 v[198:199], v152 offset:40960
	ds_read_b64_tr_b16 v[200:201], v152 offset:43008
	ds_read_b64_tr_b16 v[202:203], v152 offset:45056
	ds_read_b64_tr_b16 v[204:205], v152 offset:47104
	ds_read_b64_tr_b16 v[206:207], v152 offset:33280
	ds_read_b64_tr_b16 v[208:209], v152 offset:35328
	ds_read_b64_tr_b16 v[210:211], v152 offset:37376
	ds_read_b64_tr_b16 v[212:213], v152 offset:39424
	ds_read_b64_tr_b16 v[214:215], v152 offset:41472
	ds_read_b64_tr_b16 v[216:217], v152 offset:43520
	v_cndmask_b32_e64 v137, v137, v173, s[8:9]
	v_mul_f32_e32 v173, 0xbe0293ee, v137
	v_fmamk_f32 v82, v82, 0x3e0293ee, v173
	v_fmamk_f32 v83, v83, 0x3e0293ee, v173
	v_fmamk_f32 v84, v84, 0x3e0293ee, v173
	v_fmamk_f32 v85, v85, 0x3e0293ee, v173
	v_fmamk_f32 v86, v86, 0x3e0293ee, v173
	v_fmamk_f32 v87, v87, 0x3e0293ee, v173
	v_fmamk_f32 v88, v88, 0x3e0293ee, v173
	v_fmamk_f32 v89, v89, 0x3e0293ee, v173
	v_fmamk_f32 v90, v90, 0x3e0293ee, v173
	v_fmamk_f32 v91, v91, 0x3e0293ee, v173
	v_fmamk_f32 v92, v92, 0x3e0293ee, v173
	v_fmamk_f32 v93, v93, 0x3e0293ee, v173
	v_fmamk_f32 v94, v94, 0x3e0293ee, v173
	v_fmamk_f32 v95, v95, 0x3e0293ee, v173
	v_fmamk_f32 v96, v96, 0x3e0293ee, v173
	v_fmamk_f32 v97, v97, 0x3e0293ee, v173
	v_fmamk_f32 v66, v66, 0x3e0293ee, v173
	v_fmamk_f32 v67, v67, 0x3e0293ee, v173
	v_fmamk_f32 v68, v68, 0x3e0293ee, v173
	v_fmamk_f32 v69, v69, 0x3e0293ee, v173
	v_fmamk_f32 v70, v70, 0x3e0293ee, v173
	v_fmamk_f32 v71, v71, 0x3e0293ee, v173
	v_fmamk_f32 v72, v72, 0x3e0293ee, v173
	v_fmamk_f32 v73, v73, 0x3e0293ee, v173
	v_fmamk_f32 v74, v74, 0x3e0293ee, v173
	v_fmamk_f32 v75, v75, 0x3e0293ee, v173
	v_fmamk_f32 v76, v76, 0x3e0293ee, v173
	v_fmamk_f32 v77, v77, 0x3e0293ee, v173
	v_fmamk_f32 v78, v78, 0x3e0293ee, v173
	v_fmamk_f32 v79, v79, 0x3e0293ee, v173
	v_fmamk_f32 v80, v80, 0x3e0293ee, v173
	v_fmac_f32_e32 v173, 0x3e0293ee, v81
	v_exp_f32_e32 v81, v82
	v_exp_f32_e32 v82, v83
	v_exp_f32_e32 v83, v84
	v_exp_f32_e32 v84, v85
	v_exp_f32_e32 v85, v86
	v_exp_f32_e32 v86, v87
	v_exp_f32_e32 v87, v88
	v_exp_f32_e32 v88, v89
	v_exp_f32_e32 v89, v90
	v_exp_f32_e32 v90, v91
	v_exp_f32_e32 v91, v92
	v_exp_f32_e32 v92, v93
	v_exp_f32_e32 v93, v94
	v_exp_f32_e32 v94, v95
	v_exp_f32_e32 v95, v96
	v_exp_f32_e32 v96, v97
	v_exp_f32_e32 v97, v66
	v_add_f32_e32 v66, 0, v81
	v_add_f32_e32 v66, v82, v66
	v_add_f32_e32 v66, v83, v66
	v_add_f32_e32 v66, v84, v66
	v_add_f32_e32 v66, v85, v66
	v_add_f32_e32 v66, v86, v66
	v_add_f32_e32 v66, v87, v66
	v_add_f32_e32 v66, v88, v66
	v_add_f32_e32 v66, v89, v66
	v_add_f32_e32 v66, v90, v66
	v_add_f32_e32 v66, v91, v66
	v_add_f32_e32 v66, v92, v66
	v_add_f32_e32 v66, v93, v66
	v_exp_f32_e32 v174, v67
	v_add_f32_e32 v66, v94, v66
	v_exp_f32_e32 v175, v68
	v_add_f32_e32 v66, v95, v66
	v_exp_f32_e32 v176, v69
	v_add_f32_e32 v66, v96, v66
	v_exp_f32_e32 v177, v70
	v_add_f32_e32 v66, v97, v66
	v_exp_f32_e32 v178, v71
	v_add_f32_e32 v66, v174, v66
	v_exp_f32_e32 v179, v72
	v_add_f32_e32 v66, v175, v66
	v_exp_f32_e32 v180, v73
	v_add_f32_e32 v66, v176, v66
	v_exp_f32_e32 v181, v74
	v_add_f32_e32 v66, v177, v66
	v_exp_f32_e32 v182, v75
	v_add_f32_e32 v66, v178, v66
	v_exp_f32_e32 v183, v76
	v_add_f32_e32 v66, v179, v66
	v_exp_f32_e32 v184, v77
	v_add_f32_e32 v66, v180, v66
	v_exp_f32_e32 v185, v78
	v_add_f32_e32 v66, v181, v66
	v_exp_f32_e32 v186, v79
	v_add_f32_e32 v66, v182, v66
	v_exp_f32_e32 v187, v80
	v_add_f32_e32 v66, v183, v66
	v_exp_f32_e32 v173, v173
	v_add_f32_e32 v66, v184, v66
	v_add_f32_e32 v66, v185, v66
	v_add_f32_e32 v66, v186, v66
	v_add_f32_e32 v66, v187, v66
	v_add_f32_e32 v66, v173, v66
	v_mov_b32_e32 v67, v66
	s_nop 1
	v_permlane32_swap_b32_e32 v66, v67
	v_add_f32_e32 v188, v66, v67
	v_cvt_pk_bf16_f32 v66, v81, v82
	v_cvt_pk_bf16_f32 v67, v83, v84
	v_cvt_pk_bf16_f32 v68, v85, v86
	v_cvt_pk_bf16_f32 v69, v87, v88
	v_cvt_pk_bf16_f32 v70, v89, v90
	v_cvt_pk_bf16_f32 v71, v91, v92
	v_cvt_pk_bf16_f32 v72, v93, v94
	v_cvt_pk_bf16_f32 v73, v95, v96
	v_cvt_pk_bf16_f32 v74, v97, v174
	v_cvt_pk_bf16_f32 v75, v175, v176
	v_cvt_pk_bf16_f32 v76, v177, v178
	v_cvt_pk_bf16_f32 v77, v179, v180
	v_cvt_pk_bf16_f32 v78, v181, v182
	v_cvt_pk_bf16_f32 v79, v183, v184
	v_cvt_pk_bf16_f32 v80, v185, v186
	v_cvt_pk_bf16_f32 v81, v187, v173
	v_fmac_f32_e32 v188, v145, v171
	v_permlane32_swap_b32_e32 v66, v68
	v_permlane32_swap_b32_e32 v67, v69
	v_permlane32_swap_b32_e32 v70, v72
	v_permlane32_swap_b32_e32 v71, v73
	v_permlane32_swap_b32_e32 v74, v76
	v_permlane32_swap_b32_e32 v75, v77
	v_permlane32_swap_b32_e32 v78, v80
	v_permlane32_swap_b32_e32 v79, v81
	s_waitcnt lgkmcnt(0)
	ds_read_b64_tr_b16 v[218:219], v152 offset:45568
	ds_read_b64_tr_b16 v[220:221], v152 offset:47616
	ds_read_b64_tr_b16 v[222:223], v152 offset:33792
	ds_read_b64_tr_b16 v[224:225], v152 offset:35840
	ds_read_b64_tr_b16 v[226:227], v152 offset:37888
	ds_read_b64_tr_b16 v[228:229], v152 offset:39936
	ds_read_b64_tr_b16 v[230:231], v152 offset:41984
	ds_read_b64_tr_b16 v[232:233], v152 offset:44032
	v_mfma_f32_32x32x16_bf16 v[18:33], v[66:69], v[190:193], v[18:33]
	ds_read_b64_tr_b16 v[190:191], v152 offset:46080
	ds_read_b64_tr_b16 v[192:193], v152 offset:48128
	v_mfma_f32_32x32x16_bf16 v[18:33], v[70:73], v[194:197], v[18:33]
	ds_read_b64_tr_b16 v[194:195], v152 offset:34304
	ds_read_b64_tr_b16 v[196:197], v152 offset:36352
	v_mfma_f32_32x32x16_bf16 v[18:33], v[74:77], v[198:201], v[18:33]
	ds_read_b64_tr_b16 v[198:199], v152 offset:38400
	ds_read_b64_tr_b16 v[200:201], v152 offset:40448
	v_mfma_f32_32x32x16_bf16 v[18:33], v[78:81], v[202:205], v[18:33]
	s_waitcnt lgkmcnt(13)
; template <int DQK, int KB>
; __device__ __forceinline__ void qkt(f32x16& p0, f32x16& p1, const char* K_lds, int r32, int hi, const bf16x8* qr) {
;     constexpr int ROWB = DQK * 2, SHM_K = 64 * ROWB;
;     p0 = f32x16{}; p1 = f32x16{};
;     const char* kb[4];
; #pragma unroll
;     for (int dd = 0; dd < 4; ++dd) kb[dd] = K_lds + KB * SHM_K + r32 * ROWB + (((dd * 16 + hi * 8) * 2) ^ ((r32 & 7) << 4));
; #pragma unroll
;     for (int d0 = 0; d0 < DQK / 16; ++d0) { const char* a = kb[d0 & 3] + (d0 >> 2) * 128;
;         bf16x8 b0 = *reinterpret_cast<const bf16x8*>(a);
;         bf16x8 b1 = *reinterpret_cast<const bf16x8*>(a + 32 * ROWB);
;         p0 = __builtin_amdgcn_mfma_f32_32x32x16_bf16(b0, qr[d0], p0, 0, 0, 0);
;         p1 = __builtin_amdgcn_mfma_f32_32x32x16_bf16(b1, qr[d0], p1, 0, 0, 0); }
; template <int VB>
; __device__ __forceinline__ void pv_tile(f32x16* o, int vb0, bf16x8 pa0, bf16x8 pa1, bf16x8 pa2, bf16x8 pa3) {
;     ...
;     PV_D0(0); PV_D0(1); PV_D0(2); PV_D0(3);
	ds_read_b64_tr_b16 v[202:203], v152 offset:42496
	ds_read_b64_tr_b16 v[204:205], v152 offset:44544
	v_mfma_f32_32x32x16_bf16 v[34:49], v[66:69], v[206:209], v[34:49]
	s_waitcnt lgkmcnt(13)
	ds_read_b64_tr_b16 v[206:207], v152 offset:46592
	ds_read_b64_tr_b16 v[208:209], v152 offset:48640
	v_mfma_f32_32x32x16_bf16 v[34:49], v[70:73], v[210:213], v[34:49]
	v_mfma_f32_32x32x16_bf16 v[34:49], v[74:77], v[214:217], v[34:49]
	s_waitcnt lgkmcnt(15)
	v_mfma_f32_32x32x16_bf16 v[34:49], v[78:81], v[218:221], v[34:49]
	s_waitcnt lgkmcnt(14)
	v_mfma_f32_32x32x16_bf16 v[50:65], v[66:69], v[222:225], v[50:65]
	s_waitcnt lgkmcnt(12)
	v_mfma_f32_32x32x16_bf16 v[50:65], v[70:73], v[226:229], v[50:65]
	s_waitcnt lgkmcnt(10)
	v_mfma_f32_32x32x16_bf16 v[50:65], v[74:77], v[230:233], v[50:65]
	s_waitcnt lgkmcnt(8)
	v_mfma_f32_32x32x16_bf16 v[50:65], v[78:81], v[190:193], v[50:65]
	s_waitcnt lgkmcnt(6)
	v_mfma_f32_32x32x16_bf16 v[2:17], v[66:69], v[194:197], v[2:17]
	v_mov_b32_e32 v145, v188
	s_waitcnt lgkmcnt(4)
	v_mfma_f32_32x32x16_bf16 v[2:17], v[70:73], v[198:201], v[2:17]
	s_waitcnt lgkmcnt(2)
	v_mfma_f32_32x32x16_bf16 v[2:17], v[74:77], v[202:205], v[2:17]
	s_waitcnt lgkmcnt(0)
	v_mfma_f32_32x32x16_bf16 v[2:17], v[78:81], v[206:209], v[2:17]
	s_cmp_lt_u32 s33, 4
	s_cbranch_scc1 .LBB0_562
.LBB0_706:
	s_andn2_b64 vcc, exec, s[74:75]
	ds_read_b128 v[190:193], v166 offset:49152
	ds_read_b128 v[194:197], v166 offset:57344
	ds_read_b128 v[198:201], v167 offset:49152
	ds_read_b128 v[202:205], v167 offset:57344
	ds_read_b128 v[206:209], v168 offset:49152
	ds_read_b128 v[210:213], v168 offset:57344
	ds_read_b128 v[214:217], v169 offset:49152
	ds_read_b128 v[218:221], v169 offset:57344
	ds_read_b128 v[222:225], v166 offset:49280
	ds_read_b128 v[226:229], v166 offset:57472
	ds_read_b128 v[230:233], v167 offset:49280
	ds_read_b128 v[234:237], v167 offset:57472
	ds_read_b128 v[238:241], v168 offset:49280
	s_waitcnt lgkmcnt(12)
	v_mfma_f32_32x32x16_bf16 v[82:97], v[190:193], v[126:129], 0
	ds_read_b128 v[242:245], v168 offset:57472
	s_waitcnt lgkmcnt(12)
	v_mfma_f32_32x32x16_bf16 v[66:81], v[194:197], v[126:129], 0
	ds_read_b128 v[246:249], v169 offset:49280
	s_waitcnt lgkmcnt(12)
	v_mfma_f32_32x32x16_bf16 v[82:97], v[198:201], v[122:125], v[82:97]
	ds_read_b128 v[250:253], v169 offset:57472
	s_waitcnt lgkmcnt(12)
	v_mfma_f32_32x32x16_bf16 v[66:81], v[202:205], v[122:125], v[66:81]
	s_waitcnt lgkmcnt(11)
	v_mfma_f32_32x32x16_bf16 v[82:97], v[206:209], v[118:121], v[82:97]
	s_waitcnt lgkmcnt(10)
	v_mfma_f32_32x32x16_bf16 v[66:81], v[210:213], v[118:121], v[66:81]
	s_waitcnt lgkmcnt(9)
	v_mfma_f32_32x32x16_bf16 v[82:97], v[214:217], v[114:117], v[82:97]
	s_waitcnt lgkmcnt(8)
	v_mfma_f32_32x32x16_bf16 v[66:81], v[218:221], v[114:117], v[66:81]
	s_waitcnt lgkmcnt(7)
	v_mfma_f32_32x32x16_bf16 v[82:97], v[222:225], v[110:113], v[82:97]
	s_waitcnt lgkmcnt(6)
	v_mfma_f32_32x32x16_bf16 v[66:81], v[226:229], v[110:113], v[66:81]
	s_waitcnt lgkmcnt(5)
	v_mfma_f32_32x32x16_bf16 v[82:97], v[230:233], v[106:109], v[82:97]
	s_waitcnt lgkmcnt(4)
	v_mfma_f32_32x32x16_bf16 v[66:81], v[234:237], v[106:109], v[66:81]
	s_waitcnt lgkmcnt(3)
	v_mfma_f32_32x32x16_bf16 v[82:97], v[238:241], v[102:105], v[82:97]
	s_waitcnt lgkmcnt(2)
	v_mfma_f32_32x32x16_bf16 v[66:81], v[242:245], v[102:105], v[66:81]
	s_waitcnt lgkmcnt(1)
	v_mfma_f32_32x32x16_bf16 v[82:97], v[246:249], v[98:101], v[82:97]
	s_waitcnt lgkmcnt(0)
	v_mfma_f32_32x32x16_bf16 v[66:81], v[250:253], v[98:101], v[66:81]
	v_mov_b32_e32 v98, v151
	s_nop 0
	v_mul_f32_e32 v100, v98, v159
	v_mov_b32_e32 v105, v98
	v_mul_f32_e32 v102, 0x42000000, v98
	v_fma_f32 v104, 0, v98, v100
	v_fmac_f32_e32 v105, v105, v159
	v_pk_fma_f32 v[106:107], v[98:99], s[34:35], v[100:101] op_sel_hi:[0,1,0]
	v_pk_fma_f32 v[108:109], v[98:99], s[2:3], v[100:101] op_sel_hi:[0,1,0]
	v_pk_fma_f32 v[110:111], v[98:99], s[36:37], v[100:101] op_sel_hi:[0,1,0]
	v_pk_fma_f32 v[112:113], v[98:99], s[38:39], v[100:101] op_sel_hi:[0,1,0]
	v_pk_fma_f32 v[114:115], v[98:99], s[40:41], v[100:101] op_sel_hi:[0,1,0]
	v_pk_fma_f32 v[116:117], v[98:99], s[42:43], v[100:101] op_sel_hi:[0,1,0]
	v_pk_fma_f32 v[98:99], v[98:99], s[44:45], v[100:101] op_sel_hi:[0,1,0]
	v_pk_add_f32 v[96:97], v[96:97], v[98:99]
	v_pk_add_f32 v[92:93], v[92:93], v[114:115]
	v_pk_add_f32 v[90:91], v[90:91], v[112:113]
	v_pk_add_f32 v[88:89], v[88:89], v[110:111]
	v_pk_add_f32 v[86:87], v[86:87], v[108:109]
	v_pk_add_f32 v[84:85], v[84:85], v[106:107]
	v_pk_add_f32 v[100:101], v[102:103], v[106:107] op_sel_hi:[0,1]
	v_pk_add_f32 v[106:107], v[102:103], v[108:109] op_sel_hi:[0,1]
	v_pk_add_f32 v[108:109], v[102:103], v[110:111] op_sel_hi:[0,1]
	v_pk_add_f32 v[110:111], v[102:103], v[112:113] op_sel_hi:[0,1]
	v_pk_add_f32 v[112:113], v[102:103], v[114:115] op_sel_hi:[0,1]
	v_pk_add_f32 v[114:115], v[102:103], v[116:117] op_sel_hi:[0,1]
	v_pk_add_f32 v[98:99], v[102:103], v[98:99] op_sel_hi:[0,1]
	v_pk_add_f32 v[102:103], v[102:103], v[104:105] op_sel_hi:[0,1]
	v_pk_add_f32 v[94:95], v[94:95], v[116:117]
	v_pk_add_f32 v[82:83], v[82:83], v[104:105]
	v_pk_add_f32 v[80:81], v[80:81], v[98:99]
	v_pk_add_f32 v[78:79], v[78:79], v[114:115]
	v_pk_add_f32 v[76:77], v[76:77], v[112:113]
	v_pk_add_f32 v[74:75], v[74:75], v[110:111]
	v_pk_add_f32 v[72:73], v[72:73], v[108:109]
	v_pk_add_f32 v[70:71], v[70:71], v[106:107]
	v_pk_add_f32 v[68:69], v[68:69], v[100:101]
	v_pk_add_f32 v[66:67], v[66:67], v[102:103]
	s_cbranch_vccnz .LBB0_708
; __device__ __forceinline__ void mask_tile(f32x16& p0, f32x16& p1, int dq) {
;     const float NEG = -__builtin_inff();
; #pragma unroll
;     for (int r = 0; r < 16; ++r) {
;         const int c = (r & 3) + 8 * (r >> 2);
;         if (dq - c < 0) p0[r] = NEG;
;         if (dq - c - 32 < 0) p1[r] = NEG;
;     }
; }
	v_sub_u32_e32 v98, v132, v154
	v_add_u32_e32 v98, 0xffffff40, v98
	v_cmp_gt_i32_e64 s[66:67], 26, v98
	v_cmp_gt_i32_e64 s[68:69], 27, v98
	v_cmp_gt_i32_e64 s[64:65], 25, v98
	s_and_b64 s[66:67], s[68:69], s[66:67]
	v_cmp_gt_i32_e64 s[62:63], 24, v98
	s_and_b64 s[64:65], s[66:67], s[64:65]
	v_cmp_gt_i32_e64 s[60:61], 19, v98
	s_and_b64 s[62:63], s[64:65], s[62:63]
	v_cmp_gt_i32_e64 s[58:59], 18, v98
	s_and_b64 s[60:61], s[62:63], s[60:61]
	v_cmp_gt_i32_e64 s[56:57], 17, v98
	s_and_b64 s[58:59], s[60:61], s[58:59]
	v_cmp_gt_i32_e64 s[54:55], 16, v98
	s_and_b64 s[56:57], s[58:59], s[56:57]
	v_cmp_gt_i32_e64 s[52:53], 11, v98
	s_and_b64 s[54:55], s[56:57], s[54:55]
	v_cmp_gt_i32_e64 s[50:51], 10, v98
	s_and_b64 s[52:53], s[54:55], s[52:53]
	v_cmp_gt_i32_e64 s[48:49], 9, v98
	s_and_b64 s[50:51], s[52:53], s[50:51]
	v_cmp_gt_i32_e64 s[46:47], 8, v98
	s_and_b64 s[48:49], s[50:51], s[48:49]
	v_cmp_gt_i32_e64 s[44:45], 3, v98
	s_and_b64 s[46:47], s[48:49], s[46:47]
	v_cmp_gt_i32_e64 s[42:43], 2, v98
	s_and_b64 s[44:45], s[46:47], s[44:45]
	v_cmp_gt_i32_e64 s[40:41], 1, v98
	s_and_b64 s[42:43], s[44:45], s[42:43]
	v_cmp_gt_i32_e64 s[38:39], 0, v98
	s_and_b64 s[40:41], s[42:43], s[40:41]
	s_and_b64 s[38:39], s[40:41], s[38:39]
	v_cmp_gt_i32_e64 s[36:37], 58, v98
	v_cndmask_b32_e64 v82, v82, v147, s[38:39]
	v_cmp_gt_i32_e64 s[38:39], 59, v98
	v_cmp_gt_i32_e64 s[34:35], 57, v98
	s_and_b64 s[36:37], s[38:39], s[36:37]
	v_cmp_gt_i32_e64 s[30:31], 56, v98
	s_and_b64 s[34:35], s[36:37], s[34:35]
	v_cmp_gt_i32_e64 s[28:29], 51, v98
	s_and_b64 s[30:31], s[34:35], s[30:31]
	v_cmp_gt_i32_e64 s[26:27], 50, v98
	s_and_b64 s[28:29], s[30:31], s[28:29]
	v_cmp_gt_i32_e64 s[24:25], 49, v98
	s_and_b64 s[26:27], s[28:29], s[26:27]
	v_cmp_gt_i32_e64 s[22:23], 48, v98
	s_and_b64 s[24:25], s[26:27], s[24:25]
	v_cmp_gt_i32_e64 s[20:21], 43, v98
	s_and_b64 s[22:23], s[24:25], s[22:23]
	v_cmp_gt_i32_e64 s[18:19], 42, v98
	s_and_b64 s[20:21], s[22:23], s[20:21]
	v_cmp_gt_i32_e64 s[16:17], 41, v98
	s_and_b64 s[18:19], s[20:21], s[18:19]
	v_cmp_gt_i32_e64 s[14:15], 40, v98
	s_and_b64 s[16:17], s[18:19], s[16:17]
	v_cmp_gt_i32_e64 s[12:13], 35, v98
	s_and_b64 s[14:15], s[16:17], s[14:15]
	v_cmp_gt_i32_e64 s[10:11], 34, v98
	s_and_b64 s[12:13], s[14:15], s[12:13]
	v_cmp_gt_i32_e64 s[8:9], 33, v98
	s_and_b64 s[10:11], s[12:13], s[10:11]
	v_cmp_gt_i32_e32 vcc, 32, v98
	s_and_b64 s[8:9], s[10:11], s[8:9]
	v_cndmask_b32_e64 v85, v85, v147, s[44:45]
	s_mov_b32 s44, 0x41d00000
	v_cndmask_b32_e64 v84, v84, v147, s[42:43]
	s_mov_b32 s42, 0x41c00000
	v_cndmask_b32_e64 v83, v83, v147, s[40:41]
	s_mov_b32 s40, 0x41900000
	v_cndmask_b32_e64 v81, v81, v147, s[38:39]
	s_mov_b32 s38, 0x41800000
	v_cndmask_b32_e64 v80, v80, v147, s[36:37]
	s_mov_b32 s36, 0x41200000
	v_cndmask_b32_e64 v79, v79, v147, s[34:35]
	s_mov_b32 s34, 2.0
	s_and_b64 vcc, s[8:9], vcc
	v_cndmask_b32_e64 v97, v97, v147, s[68:69]
	v_cndmask_b32_e64 v96, v96, v147, s[66:67]
	v_cndmask_b32_e64 v95, v95, v147, s[64:65]
	v_cndmask_b32_e64 v94, v94, v147, s[62:63]
	v_cndmask_b32_e64 v93, v93, v147, s[60:61]
	v_cndmask_b32_e64 v92, v92, v147, s[58:59]
	v_cndmask_b32_e64 v91, v91, v147, s[56:57]
	v_cndmask_b32_e64 v90, v90, v147, s[54:55]
	v_cndmask_b32_e64 v89, v89, v147, s[52:53]
	v_cndmask_b32_e64 v88, v88, v147, s[50:51]
	v_cndmask_b32_e64 v87, v87, v147, s[48:49]
	v_cndmask_b32_e64 v86, v86, v147, s[46:47]
	s_mov_b32 s45, 0x41d80000
	s_mov_b32 s43, 0x41c80000
	s_mov_b32 s41, 0x41980000
	s_mov_b32 s39, 0x41880000
	s_mov_b32 s37, 0x41300000
	s_mov_b32 s35, 0x40400000
	v_cndmask_b32_e64 v78, v78, v147, s[30:31]
	v_cndmask_b32_e64 v77, v77, v147, s[28:29]
	v_cndmask_b32_e64 v76, v76, v147, s[26:27]
	v_cndmask_b32_e64 v75, v75, v147, s[24:25]
	v_cndmask_b32_e64 v74, v74, v147, s[22:23]
	v_cndmask_b32_e64 v73, v73, v147, s[20:21]
	v_cndmask_b32_e64 v72, v72, v147, s[18:19]
	v_cndmask_b32_e64 v71, v71, v147, s[16:17]
	v_cndmask_b32_e64 v70, v70, v147, s[14:15]
	v_cndmask_b32_e64 v69, v69, v147, s[12:13]
	v_cndmask_b32_e64 v68, v68, v147, s[10:11]
	v_cndmask_b32_e64 v67, v67, v147, s[8:9]
	v_cndmask_b32_e32 v66, v66, v147, vcc

; template <int DQK> __device__ __forceinline__ void partialSM(f32x16& p0, f32x16& p1, float& m_reg, float& mn, float& alpha) {
;     ...
;     for (int r = 0; r < 16; ++r) p0[r] = fmaf(p0[r], C2, mnL);
; #pragma unroll
;     for (int r = 0; r < 16; ++r) p1[r] = fmaf(p1[r], C2, mnL);
; #pragma unroll
;     for (int r = 0; r < 16; ++r) p0[r] = __builtin_amdgcn_exp2f(p0[r]);
; }
; __device__ __forceinline__ void finishSM(f32x16& p0, f32x16& p1, float alpha, float& l_reg, bf16x8& pa0, bf16x8& pa1, bf16x8& pa2, bf16x8& pa3) {
; #pragma unroll
;     for (int r = 0; r < 16; ++r) p1[r] = __builtin_amdgcn_exp2f(p1[r]);
;     float ps = 0;
; #pragma unroll
;     for (int r = 0; r < 16; ++r) ps += p0[r];
; #pragma unroll
;     for (int r = 0; r < 16; ++r) ps += p1[r];
;     { auto rr = __builtin_amdgcn_permlane32_swap(__float_as_uint(ps), __float_as_uint(ps), false, false);
;       ps = __uint_as_float(rr[0]) + __uint_as_float(rr[1]); }
;     l_reg = l_reg * alpha + ps;
;     ...
;     PK4(p0, 0, pa0); PK4(p0, 8, pa1); PK4(p1, 0, pa2); PK4(p1, 8, pa3);
;     ...
; }
; template <int VB>
; __device__ __forceinline__ void pv_tile(f32x16* o, int vb0, bf16x8 pa0, bf16x8 pa1, bf16x8 pa2, bf16x8 pa3) {
;     ...
;     PV_D0(0); PV_D0(1); PV_D0(2); PV_D0(3);
.LBB0_712:
	ds_read_b64_tr_b16 v[190:191], v152 offset:49152
	ds_read_b64_tr_b16 v[192:193], v152 offset:51200
	ds_read_b64_tr_b16 v[194:195], v152 offset:53248
	ds_read_b64_tr_b16 v[196:197], v152 offset:55296
	ds_read_b64_tr_b16 v[198:199], v152 offset:57344
	ds_read_b64_tr_b16 v[200:201], v152 offset:59392
	ds_read_b64_tr_b16 v[202:203], v152 offset:61440
	ds_read_b64_tr_b16 v[204:205], v152 offset:63488
	ds_read_b64_tr_b16 v[206:207], v152 offset:49664
	ds_read_b64_tr_b16 v[208:209], v152 offset:51712
	ds_read_b64_tr_b16 v[210:211], v152 offset:53760
	ds_read_b64_tr_b16 v[212:213], v152 offset:55808
	ds_read_b64_tr_b16 v[214:215], v152 offset:57856
	ds_read_b64_tr_b16 v[216:217], v152 offset:59904
	v_cndmask_b32_e64 v137, v137, v99, s[8:9]
	v_mul_f32_e32 v99, 0xbe0293ee, v137
	v_fmamk_f32 v82, v82, 0x3e0293ee, v99
	v_fmamk_f32 v83, v83, 0x3e0293ee, v99
	v_fmamk_f32 v84, v84, 0x3e0293ee, v99
	v_fmamk_f32 v85, v85, 0x3e0293ee, v99
	v_fmamk_f32 v86, v86, 0x3e0293ee, v99
	v_fmamk_f32 v87, v87, 0x3e0293ee, v99
	v_fmamk_f32 v88, v88, 0x3e0293ee, v99
	v_fmamk_f32 v89, v89, 0x3e0293ee, v99
	v_fmamk_f32 v90, v90, 0x3e0293ee, v99
	v_fmamk_f32 v91, v91, 0x3e0293ee, v99
	v_fmamk_f32 v92, v92, 0x3e0293ee, v99
	v_fmamk_f32 v93, v93, 0x3e0293ee, v99
	v_fmamk_f32 v94, v94, 0x3e0293ee, v99
	v_fmamk_f32 v95, v95, 0x3e0293ee, v99
	v_fmamk_f32 v96, v96, 0x3e0293ee, v99
	v_fmamk_f32 v97, v97, 0x3e0293ee, v99
	v_fmamk_f32 v66, v66, 0x3e0293ee, v99
	v_fmamk_f32 v67, v67, 0x3e0293ee, v99
	v_fmamk_f32 v68, v68, 0x3e0293ee, v99
	v_fmamk_f32 v69, v69, 0x3e0293ee, v99
	v_fmamk_f32 v70, v70, 0x3e0293ee, v99
	v_fmamk_f32 v71, v71, 0x3e0293ee, v99
	v_fmamk_f32 v72, v72, 0x3e0293ee, v99
	v_fmamk_f32 v73, v73, 0x3e0293ee, v99
	v_fmamk_f32 v74, v74, 0x3e0293ee, v99
	v_fmamk_f32 v75, v75, 0x3e0293ee, v99
	v_fmamk_f32 v76, v76, 0x3e0293ee, v99
	v_fmamk_f32 v77, v77, 0x3e0293ee, v99
	v_fmamk_f32 v78, v78, 0x3e0293ee, v99
	v_fmamk_f32 v79, v79, 0x3e0293ee, v99
	v_fmamk_f32 v80, v80, 0x3e0293ee, v99
	v_fmac_f32_e32 v99, 0x3e0293ee, v81
	v_exp_f32_e32 v81, v82
	v_exp_f32_e32 v82, v83
	v_exp_f32_e32 v83, v84
	v_exp_f32_e32 v84, v85
	v_exp_f32_e32 v85, v86
	v_exp_f32_e32 v86, v87
	v_exp_f32_e32 v87, v88
	v_exp_f32_e32 v88, v89
	v_exp_f32_e32 v89, v90
	v_exp_f32_e32 v90, v91
	v_exp_f32_e32 v91, v92
	v_exp_f32_e32 v92, v93
	v_exp_f32_e32 v93, v94
	v_exp_f32_e32 v94, v95
	v_exp_f32_e32 v95, v96
	v_exp_f32_e32 v96, v97
	v_exp_f32_e32 v97, v66
	v_add_f32_e32 v66, 0, v81
	v_add_f32_e32 v66, v82, v66
	v_add_f32_e32 v66, v83, v66
	v_add_f32_e32 v66, v84, v66
	v_add_f32_e32 v66, v85, v66
	v_add_f32_e32 v66, v86, v66
	v_add_f32_e32 v66, v87, v66
	v_add_f32_e32 v66, v88, v66
	v_add_f32_e32 v66, v89, v66
	v_add_f32_e32 v66, v90, v66
	v_add_f32_e32 v66, v91, v66
	v_add_f32_e32 v66, v92, v66
	v_add_f32_e32 v66, v93, v66
	v_exp_f32_e32 v100, v67
	v_add_f32_e32 v66, v94, v66
	v_exp_f32_e32 v101, v68
	v_add_f32_e32 v66, v95, v66
	v_exp_f32_e32 v102, v69
	v_add_f32_e32 v66, v96, v66
	v_exp_f32_e32 v103, v70
	v_add_f32_e32 v66, v97, v66
	v_exp_f32_e32 v104, v71
	v_add_f32_e32 v66, v100, v66
	v_exp_f32_e32 v105, v72
	v_add_f32_e32 v66, v101, v66
	v_exp_f32_e32 v106, v73
	v_add_f32_e32 v66, v102, v66
	v_exp_f32_e32 v107, v74
	v_add_f32_e32 v66, v103, v66
	v_exp_f32_e32 v108, v75
	v_add_f32_e32 v66, v104, v66
	v_exp_f32_e32 v109, v76
	v_add_f32_e32 v66, v105, v66
	v_exp_f32_e32 v110, v77
	v_add_f32_e32 v66, v106, v66
	v_exp_f32_e32 v111, v78
	v_add_f32_e32 v66, v107, v66
	v_exp_f32_e32 v112, v79
	v_add_f32_e32 v66, v108, v66
	v_exp_f32_e32 v113, v80
	v_add_f32_e32 v66, v109, v66
	v_exp_f32_e32 v99, v99
	v_add_f32_e32 v66, v110, v66
	v_add_f32_e32 v66, v111, v66
	v_add_f32_e32 v66, v112, v66
	v_add_f32_e32 v66, v113, v66
	v_add_f32_e32 v66, v99, v66
	v_mov_b32_e32 v67, v66
	s_nop 1
	v_permlane32_swap_b32_e32 v66, v67
	v_add_f32_e32 v114, v66, v67
	v_cvt_pk_bf16_f32 v66, v81, v82
	v_cvt_pk_bf16_f32 v67, v83, v84
	v_cvt_pk_bf16_f32 v68, v85, v86
	v_cvt_pk_bf16_f32 v69, v87, v88
	v_cvt_pk_bf16_f32 v70, v89, v90
	v_cvt_pk_bf16_f32 v71, v91, v92
	v_cvt_pk_bf16_f32 v72, v93, v94
	v_cvt_pk_bf16_f32 v73, v95, v96
	v_cvt_pk_bf16_f32 v74, v97, v100
	v_cvt_pk_bf16_f32 v75, v101, v102
	v_cvt_pk_bf16_f32 v76, v103, v104
	v_cvt_pk_bf16_f32 v77, v105, v106
	v_cvt_pk_bf16_f32 v78, v107, v108
	v_cvt_pk_bf16_f32 v79, v109, v110
	v_cvt_pk_bf16_f32 v80, v111, v112
	v_cvt_pk_bf16_f32 v81, v113, v99
	v_fmac_f32_e32 v114, v145, v98
	v_permlane32_swap_b32_e32 v66, v68
	v_permlane32_swap_b32_e32 v67, v69
	v_permlane32_swap_b32_e32 v70, v72
	v_permlane32_swap_b32_e32 v71, v73
	v_permlane32_swap_b32_e32 v74, v76
	v_permlane32_swap_b32_e32 v75, v77
	v_permlane32_swap_b32_e32 v78, v80
	v_permlane32_swap_b32_e32 v79, v81
	s_waitcnt lgkmcnt(0)
	ds_read_b64_tr_b16 v[218:219], v152 offset:61952
	ds_read_b64_tr_b16 v[220:221], v152 offset:64000
	ds_read_b64_tr_b16 v[222:223], v152 offset:50176
	ds_read_b64_tr_b16 v[224:225], v152 offset:52224
	ds_read_b64_tr_b16 v[226:227], v152 offset:54272
	ds_read_b64_tr_b16 v[228:229], v152 offset:56320
	ds_read_b64_tr_b16 v[230:231], v152 offset:58368
	ds_read_b64_tr_b16 v[232:233], v152 offset:60416
	v_mfma_f32_32x32x16_bf16 v[18:33], v[66:69], v[190:193], v[18:33]
	ds_read_b64_tr_b16 v[190:191], v152 offset:62464
	ds_read_b64_tr_b16 v[192:193], v152 offset:64512
	v_mfma_f32_32x32x16_bf16 v[18:33], v[70:73], v[194:197], v[18:33]
	ds_read_b64_tr_b16 v[194:195], v152 offset:50688
	ds_read_b64_tr_b16 v[196:197], v152 offset:52736
	v_mfma_f32_32x32x16_bf16 v[18:33], v[74:77], v[198:201], v[18:33]
	ds_read_b64_tr_b16 v[198:199], v152 offset:54784
	ds_read_b64_tr_b16 v[200:201], v152 offset:56832
	v_mfma_f32_32x32x16_bf16 v[18:33], v[78:81], v[202:205], v[18:33]
	s_waitcnt lgkmcnt(13)
	ds_read_b64_tr_b16 v[202:203], v152 offset:58880
	ds_read_b64_tr_b16 v[204:205], v152 offset:60928
	v_mfma_f32_32x32x16_bf16 v[34:49], v[66:69], v[206:209], v[34:49]
	s_waitcnt lgkmcnt(13)
	ds_read_b64_tr_b16 v[206:207], v152 offset:62976
	ds_read_b64_tr_b16 v[208:209], v152 offset:65024
	v_mfma_f32_32x32x16_bf16 v[34:49], v[70:73], v[210:213], v[34:49]
	v_mfma_f32_32x32x16_bf16 v[34:49], v[74:77], v[214:217], v[34:49]
	s_waitcnt lgkmcnt(15)
	v_mfma_f32_32x32x16_bf16 v[34:49], v[78:81], v[218:221], v[34:49]
	s_waitcnt lgkmcnt(14)
	v_mfma_f32_32x32x16_bf16 v[50:65], v[66:69], v[222:225], v[50:65]
	s_waitcnt lgkmcnt(12)
	v_mfma_f32_32x32x16_bf16 v[50:65], v[70:73], v[226:229], v[50:65]
	s_waitcnt lgkmcnt(10)
	v_mfma_f32_32x32x16_bf16 v[50:65], v[74:77], v[230:233], v[50:65]
	s_waitcnt lgkmcnt(8)
	v_mfma_f32_32x32x16_bf16 v[50:65], v[78:81], v[190:193], v[50:65]
	s_waitcnt lgkmcnt(6)
	v_mfma_f32_32x32x16_bf16 v[2:17], v[66:69], v[194:197], v[2:17]
	v_mov_b32_e32 v145, v114
	s_waitcnt lgkmcnt(4)
	v_mfma_f32_32x32x16_bf16 v[2:17], v[70:73], v[198:201], v[2:17]
	s_waitcnt lgkmcnt(2)
	v_mfma_f32_32x32x16_bf16 v[2:17], v[74:77], v[202:205], v[2:17]
	s_waitcnt lgkmcnt(0)
	v_mfma_f32_32x32x16_bf16 v[2:17], v[78:81], v[206:209], v[2:17]
	s_and_saveexec_b64 s[8:9], s[4:5]
	s_cbranch_execnz .LBB0_563
; __device__ __forceinline__ void p4_moba_loop(Frame& F, const Args& A, const int qo, const bool cvmode) {
;     ...
;             MB_STEP(0); MB_STEP(1); MB_STEP(2); MB_STEP(3);
;     ...
;             if (hi == 0) { ws[r32] = l_reg;
	s_branch .LBB0_564

; #define LAS __attribute__((address_space(3)))
; template <int MODE> __device__ __forceinline__ void cv_finish(const f32x4 (&tv)[16], int K, int nblk, unsigned char* WT, int item, int lane) {
;     const int kb = item / nblk, nb = item - kb * nblk, k0 = 64 * kb + 16 * (lane >> 4), n0 = 64 * nb + 4 * (lane & 15);
;     unsigned D[16];
; #pragma unroll
;     for (int i = 0; i < 16; ++i) { const f32x2 a = (f32x2){tv[i].x, tv[i].y} * (f32x2){1024.f, 1024.f}, b = (f32x2){tv[i].z, tv[i].w} * (f32x2){1024.f, 1024.f};
;         D[i] = pk4_fp8(a.x, a.y, b.x, b.y); }
;     unsigned O[4][4];
; #pragma unroll
;     for (int q = 0; q < 4; ++q) { const unsigned a = D[4 * q], b = D[4 * q + 1], c = D[4 * q + 2], d = D[4 * q + 3];
;         const unsigned t0 = __builtin_amdgcn_perm(b, a, 0x05010400u), t1 = __builtin_amdgcn_perm(b, a, 0x07030602u), u0 = __builtin_amdgcn_perm(d, c, 0x05010400u), u1 = __builtin_amdgcn_perm(d, c, 0x07030602u);
;         O[0][q] = __builtin_amdgcn_perm(u0, t0, 0x05040100u); O[1][q] = __builtin_amdgcn_perm(u0, t0, 0x07060302u); O[2][q] = __builtin_amdgcn_perm(u1, t1, 0x05040100u); O[3][q] = __builtin_amdgcn_perm(u1, t1, 0x07060302u); }
; #pragma unroll
;     for (int j = 0; j < 4; ++j) { u32x4 o; o.x = O[j][0]; o.y = O[j][1]; o.z = O[j][2]; o.w = O[j][3];
;         __builtin_nontemporal_store(o, (u32x4*)(WT + (size_t)drow<MODE>(n0 + j) * K + k0)); }
; }
; __device__ __forceinline__ void conv_wave(Frame& F, const Args& A, volatile LAS unsigned* done = nullptr) {
;     for (;;) {
;         if (done) { if (__builtin_amdgcn_readfirstlane((int)*done) >= 4) break; }
;         unsigned u = 0u; if (F.lane == 0) u = __hip_atomic_fetch_add(F.ctl + CW_CQ, 1u, RLX_AGENT);
;         const int c = __builtin_amdgcn_readfirstlane((int)u);
;         if (c >= CV_NGRP) break;
;         const int r0 = c * 4;
;         if (r0 < NE * CV_I_W1E) { const int e = r0 / CV_I_W1E;
;             cv_run4<2>(IN_F(13) + (size_t)e * DM * 2 * FF, DM, 2 * FF, WSP(unsigned char, WS_W1) + (size_t)e * 2 * FF * DM, r0 - e * CV_I_W1E, F.lane); }
;         else { const int r = r0 - NE * CV_I_W1E, e = r / CV_I_W2E;
;             cv_run4<0>(IN_F(15) + (size_t)e * FF * DM, FF, DM, WSP(unsigned char, WS_W2) + (size_t)e * DM * FF, r - e * CV_I_W2E, F.lane); }
;     }
; }
.LBB0_750:
	v_readlane_b32 s0, v254, 52
	v_readlane_b32 s1, v254, 53
	s_andn2_b64 vcc, exec, s[0:1]
	s_cbranch_vccnz .LBB0_782
	s_mov_b32 s3, 0
	v_mov_b32_e32 v67, 0
	s_movk_i32 s0, 0x2000
	s_movk_i32 s1, 0x4000
	s_movk_i32 s5, 0x6000
	s_mov_b32 s12, 0x8000
	s_mov_b32 s13, 0xa000
	s_mov_b32 s14, 0xc000
	s_mov_b32 s15, 0xe000
	s_mov_b32 s16, 0x10000
	s_mov_b32 s17, 0x12000
	s_mov_b32 s18, 0x14000
	s_mov_b32 s19, 0x16000
	s_mov_b32 s20, 0x18000
	s_mov_b32 s21, 0x1a000
	s_mov_b32 s22, 0x1c000
	s_mov_b32 s23, 0x1e000
	s_mov_b32 s4, 0x44800000
	s_mov_b32 s24, 0xc3e00000
	s_mov_b32 s25, 0x5010400
	s_mov_b32 s26, 0x7030602
	s_mov_b32 s27, 0x5040100
	s_mov_b32 s28, 0x7060302
	s_mov_b32 s29, 0x20000
	s_mov_b32 s30, 0x24000
	s_mov_b32 s31, 0x28000
	s_mov_b32 s33, 0x2c000
	s_mov_b32 s34, 0x30000
	s_mov_b32 s35, 0x34000
	s_movk_i32 s36, 0x7ff
	s_movk_i32 s37, 0x80
	s_movk_i32 s38, 0xff00
	v_lshlrev_b32_e32 v66, 2, v130
	v_mov_b32_e32 v72, 0x43e00000
	s_branch .LBB0_754

; __device__ __forceinline__ void p4_mla_loop(Frame& F, const Args& A, const int qo) {
;     ...
;     for (;;) {
;         __syncthreads();
;         if (tid == 0) F.MISC[16] = __hip_atomic_fetch_add(F.ctl + CW_QUEUE + qo, 1u, RLX_AGENT);
;         __syncthreads();
.LBB0_786:
	s_barrier
	s_and_saveexec_b64 s[4:5], s[0:1]
	s_cbranch_execz .LBB0_790
	s_mov_b64 s[8:9], exec
	v_mbcnt_lo_u32_b32 v2, s8, 0
	v_mbcnt_hi_u32_b32 v2, s9, v2
	v_cmp_eq_u32_e32 vcc, 0, v2
	s_and_saveexec_b64 s[6:7], vcc
	s_cbranch_execz .LBB0_789
	s_bcnt1_i32_b64 s8, s[8:9]
	v_mov_b32_e32 v4, s8
	global_atomic_add v4, v3, v4, s[94:95] offset:256 sc0

; #define VM_WAIT() asm volatile("s_waitcnt vmcnt(0)" ::: "memory")
; #define A_SWRITE(bf) do { *(bf16x8*)(K_lds + (bf) * SHM_K + kws) = st_k0; *(bf16x8*)(K_lds + (bf) * SHM_K + kws + 32 * ROWB) = st_k1; \
;         if constexpr (DQK == 192) *(bf16x8*)(K_lds + (bf) * SHM_K + kws2) = st_k2; \
;         *(bf16x8*)(V_lds + (bf) * SHM_V + vst0) = st_v0; *(bf16x8*)(V_lds + (bf) * SHM_V + vst1) = st_v1; } while (0)
; template <int DQK, bool BIAS> ...
;     ...
;     const unsigned goff = (unsigned)(sr * (int)kpitch + sc) * 2u, goff2 = (unsigned)(rr_ * 64 + rc) * 2u;
;     bf16x8 st_k0, st_k1, st_k2 = {}, st_v0, st_v1;
;     ...
;     m_reg = -1e30f; l_reg = 0.f;
; #pragma unroll
;     for (int d = 0; d < 4; ++d) o[d] = f32x16{};
;     A_SLOAD(kb0); VM_WAIT(); A_SWRITE(0);
;     if (NT > 1) { A_SLOAD(kb0 + 64); VM_WAIT(); A_SWRITE(1); }
;     __syncthreads();
; __device__ __forceinline__ void p4_mla_loop(Frame& F, const Args& A, const int qo) {
;     ...
;         __syncthreads();
;         if (tid == 0) F.MISC[16] = __hip_atomic_fetch_add(F.ctl + CW_QUEUE + qo, 1u, RLX_AGENT);
;         __syncthreads();
;         const int it = __builtin_amdgcn_readfirstlane((int)F.MISC[16]);
;         if (it >= 512) break;
;         int ln = lane; asm volatile("" : "+v"(ln)); const int r32 = ln & 31, hi = ln >> 5;
;         const int qb = 31 - (it >> 4), bh = it & 15, b = bh >> 3, h = bh & 7;
;         const int m0 = b * SEQ + qb * 256 + wid * 32;
;         bf16x8 qr[12];
;         { const bf16_t* qp = WSP(bf16_t, WS_QF) + (size_t)(m0 + r32) * QFW + h * 192 + hi * 8;
; #pragma unroll
;           for (int d0 = 0; d0 < 12; ++d0) qr[d0] = *(const bf16x8*)(qp + d0 * 16); }
.LBB0_790:
	s_or_b64 exec, exec, s[4:5]
	s_waitcnt lgkmcnt(0)
	s_barrier
	ds_read_b32 v2, v191
	s_mov_b64 s[4:5], -1
	s_waitcnt lgkmcnt(0)
	v_readfirstlane_b32 s6, v2
	s_cmpk_lt_i32 s6, 0x200
	s_cbranch_scc0 .LBB0_785
	s_ashr_i32 s5, s6, 4
	s_lshl_b32 s4, s6, 10
	s_and_b32 s83, s6, 7
	s_and_b32 s8, s4, 0x2000
	s_lshl_b32 s4, s5, 8
	v_readlane_b32 s6, v254, 38
	s_sub_i32 s84, s6, s4
	v_mov_b32_e32 v200, v170
	s_addk_i32 s84, 0x1f00
	s_add_i32 s74, s84, s8
	v_and_b32_e32 v202, 31, v200
	v_or_b32_e32 v2, s74, v202
	v_mov_b64_e32 v[4:5], s[70:71]
	s_movk_i32 s6, 0xc00
	v_mad_i64_i32 v[4:5], s[6:7], v2, s6, v[4:5]
	s_lshl_b32 s6, s8, 12
	v_readlane_b32 s7, v255, 18
	s_add_u32 s6, s7, s6
	v_readlane_b32 s7, v255, 15
	v_ashrrev_i32_e32 v201, 5, v200
	s_addc_u32 s7, s7, 0
	s_lshl_b32 s9, s83, 9
	s_mul_i32 s68, s83, 0x180
	v_lshlrev_b32_e32 v6, 3, v201
	s_add_u32 s76, s6, s9
	v_lshl_add_u64 v[4:5], v[4:5], 0, s[68:69]
	v_ashrrev_i32_e32 v7, 31, v6
	s_addc_u32 s77, s7, 0
	s_lshl_b32 s6, s8, 7
	v_readlane_b32 s7, v255, 20
	v_lshl_add_u64 v[20:21], v[6:7], 1, v[4:5]
	s_add_u32 s6, s7, s6
	v_readlane_b32 s7, v255, 19
	v_lshl_add_u64 v[24:25], s[76:77], 0, v[174:175]
	global_load_dwordx4 v[154:157], v[20:21], off offset:32
	global_load_dwordx4 v[150:153], v[20:21], off offset:64
	global_load_dwordx4 v[142:145], v[20:21], off offset:96
	global_load_dwordx4 v[138:141], v[20:21], off offset:128
	global_load_dwordx4 v[134:137], v[20:21], off offset:160
	global_load_dwordx4 v[130:133], v[20:21], off offset:192
	global_load_dwordx4 v[126:129], v[20:21], off offset:224
	global_load_dwordx4 v[122:125], v[20:21], off offset:256
	global_load_dwordx4 v[118:121], v[20:21], off offset:288
	global_load_dwordx4 v[114:117], v[20:21], off offset:320
	s_addc_u32 s7, s7, 0
	v_add_co_u32_e32 v16, vcc, s96, v24
	v_lshl_add_u64 v[178:179], s[6:7], 0, v[176:177]
	s_nop 0
	v_addc_co_u32_e32 v17, vcc, 0, v25, vcc
	s_mov_b32 s6, 0x40000
	v_add_co_u32_e32 v36, vcc, s6, v24
	s_mov_b32 s6, 0x60000
	s_nop 0
	v_addc_co_u32_e32 v37, vcc, 0, v25, vcc
	global_load_dwordx4 v[4:7], v[16:17], off offset:256
	global_load_dwordx4 v[146:149], v[20:21], off offset:352
	global_load_dwordx4 v[8:11], v[24:25], off
	global_load_dwordx4 v[12:15], v[24:25], off offset:256
	s_nop 0
	global_load_dwordx4 v[16:19], v[16:17], off
	s_nop 0
	global_load_dwordx4 v[158:161], v[20:21], off
	s_nop 0
	global_load_dwordx4 v[20:23], v[178:179], off
	v_add_co_u32_e32 v40, vcc, s6, v24
	s_movk_i32 s6, 0x2000
	s_nop 0
	v_addc_co_u32_e32 v41, vcc, 0, v25, vcc
	v_add_co_u32_e32 v32, vcc, s6, v178
	s_waitcnt vmcnt(0)
	global_load_dwordx4 v[24:27], v[36:37], off
	global_load_dwordx4 v[28:31], v[40:41], off
	v_addc_co_u32_e32 v33, vcc, 0, v179, vcc
	global_load_dwordx4 v[32:35], v[32:33], off
	s_nop 0
	global_load_dwordx4 v[36:39], v[36:37], off offset:256
	s_nop 0
	global_load_dwordx4 v[40:43], v[40:41], off offset:256
	v_readfirstlane_b32 s75, v0
	s_cmpk_lt_u32 s75, 0x100
	s_waitcnt vmcnt(9)
	ds_write_b128 v192, v[8:11] offset:49152
	s_waitcnt vmcnt(7)
	ds_write_b128 v192, v[16:19] offset:61440
	s_waitcnt vmcnt(5)
	ds_write_b128 v193, v[20:23] offset:49408
	ds_write_b128 v194, v[12:15]
	ds_write_b128 v195, v[4:7]
	s_waitcnt vmcnt(0)
	s_waitcnt vmcnt(4)
	ds_write_b128 v196, v[24:27]
	s_waitcnt vmcnt(3)
	ds_write_b128 v196, v[28:31] offset:12288
	s_waitcnt vmcnt(2)
	ds_write_b128 v197, v[32:35]
	s_waitcnt vmcnt(1)
	ds_write_b128 v194, v[36:39] offset:16384
	s_waitcnt vmcnt(0)
	ds_write_b128 v195, v[40:43] offset:16384
	s_waitcnt lgkmcnt(0)
	s_barrier
	s_cbranch_scc1 .LBB0_793
	s_waitcnt lgkmcnt(0)
	s_barrier

; template <int DQK> __device__ __forceinline__ void partialSM(f32x16& p0, f32x16& p1, float& m_reg, float& mn, float& alpha) {
;     ...
;     for (int r = 0; r < 16; ++r) p0[r] = fmaf(p0[r], C2, mnL);
; #pragma unroll
;     for (int r = 0; r < 16; ++r) p1[r] = fmaf(p1[r], C2, mnL);
; #pragma unroll
;     for (int r = 0; r < 16; ++r) p0[r] = __builtin_amdgcn_exp2f(p0[r]);
; }
; __device__ __forceinline__ void finishSM(f32x16& p0, f32x16& p1, float alpha, float& l_reg, bf16x8& pa0, bf16x8& pa1, bf16x8& pa2, bf16x8& pa3) {
; #pragma unroll
;     for (int r = 0; r < 16; ++r) p1[r] = __builtin_amdgcn_exp2f(p1[r]);
;     float ps = 0;
; #pragma unroll
;     for (int r = 0; r < 16; ++r) ps += p0[r];
; #pragma unroll
;     for (int r = 0; r < 16; ++r) ps += p1[r];
;     { auto rr = __builtin_amdgcn_permlane32_swap(__float_as_uint(ps), __float_as_uint(ps), false, false);
;       ps = __uint_as_float(rr[0]) + __uint_as_float(rr[1]); }
;     l_reg = l_reg * alpha + ps;
;     ...
;     PK4(p0, 0, pa0); PK4(p0, 8, pa1); PK4(p1, 0, pa2); PK4(p1, 8, pa3);
;     ...
; }
; template <int VB>
; __device__ __forceinline__ void pv_tile(f32x16* o, int vb0, bf16x8 pa0, bf16x8 pa1, bf16x8 pa2, bf16x8 pa3) {
;     ...
;     PV_D0(0); PV_D0(1); PV_D0(2); PV_D0(3);
.LBB0_801:
	ds_read_b64_tr_b16 v[218:219], v181 offset:0
	ds_read_b64_tr_b16 v[220:221], v181 offset:2048
	ds_read_b64_tr_b16 v[222:223], v181 offset:4096
	ds_read_b64_tr_b16 v[224:225], v181 offset:6144
	ds_read_b64_tr_b16 v[226:227], v181 offset:8192
	ds_read_b64_tr_b16 v[228:229], v181 offset:10240
	ds_read_b64_tr_b16 v[230:231], v181 offset:12288
	ds_read_b64_tr_b16 v[232:233], v181 offset:14336
	ds_read_b64_tr_b16 v[234:235], v181 offset:512
	ds_read_b64_tr_b16 v[236:237], v181 offset:2560
	ds_read_b64_tr_b16 v[238:239], v181 offset:4608
	ds_read_b64_tr_b16 v[240:241], v181 offset:6656
	ds_read_b64_tr_b16 v[242:243], v181 offset:8704
	ds_read_b64_tr_b16 v[244:245], v181 offset:10752
	v_cndmask_b32_e64 v216, v216, v17, s[4:5]
	v_mul_f32_e32 v17, 0xbdd53b94, v216
	v_fmamk_f32 v82, v82, 0x3dd53b94, v17
	v_fmamk_f32 v83, v83, 0x3dd53b94, v17
	v_exp_f32_e32 v82, v82
	v_fmamk_f32 v84, v84, 0x3dd53b94, v17
	v_exp_f32_e32 v83, v83
	v_fmamk_f32 v85, v85, 0x3dd53b94, v17
	v_exp_f32_e32 v84, v84
	v_fmamk_f32 v86, v86, 0x3dd53b94, v17
	v_exp_f32_e32 v85, v85
	v_fmamk_f32 v87, v87, 0x3dd53b94, v17
	v_fmamk_f32 v88, v88, 0x3dd53b94, v17
	v_fmamk_f32 v89, v89, 0x3dd53b94, v17
	v_fmamk_f32 v90, v90, 0x3dd53b94, v17
	v_fmamk_f32 v91, v91, 0x3dd53b94, v17
	v_fmamk_f32 v92, v92, 0x3dd53b94, v17
	v_fmamk_f32 v93, v93, 0x3dd53b94, v17
	v_fmamk_f32 v94, v94, 0x3dd53b94, v17
	v_fmamk_f32 v95, v95, 0x3dd53b94, v17
	v_fmamk_f32 v96, v96, 0x3dd53b94, v17
	v_fmamk_f32 v97, v97, 0x3dd53b94, v17
	v_fmamk_f32 v98, v98, 0x3dd53b94, v17
	v_fmamk_f32 v99, v99, 0x3dd53b94, v17
	v_fmamk_f32 v100, v100, 0x3dd53b94, v17
	v_fmamk_f32 v101, v101, 0x3dd53b94, v17
	v_fmamk_f32 v102, v102, 0x3dd53b94, v17
	v_fmamk_f32 v103, v103, 0x3dd53b94, v17
	v_fmamk_f32 v104, v104, 0x3dd53b94, v17
	v_fmamk_f32 v105, v105, 0x3dd53b94, v17
	v_fmamk_f32 v106, v106, 0x3dd53b94, v17
	v_fmamk_f32 v107, v107, 0x3dd53b94, v17
	v_fmamk_f32 v108, v108, 0x3dd53b94, v17
	v_fmamk_f32 v109, v109, 0x3dd53b94, v17
	v_fmamk_f32 v110, v110, 0x3dd53b94, v17
	v_fmamk_f32 v111, v111, 0x3dd53b94, v17
	v_fmamk_f32 v112, v112, 0x3dd53b94, v17
	v_fmac_f32_e32 v17, 0x3dd53b94, v113
	v_exp_f32_e32 v86, v86
	v_add_f32_e32 v113, 0, v82
	v_exp_f32_e32 v87, v87
	v_add_f32_e32 v113, v83, v113
	v_exp_f32_e32 v88, v88
	v_add_f32_e32 v113, v84, v113
	v_exp_f32_e32 v89, v89
	v_add_f32_e32 v113, v85, v113
	v_exp_f32_e32 v90, v90
	v_add_f32_e32 v113, v86, v113
	v_exp_f32_e32 v91, v91
	v_add_f32_e32 v113, v87, v113
	v_exp_f32_e32 v92, v92
	v_add_f32_e32 v113, v88, v113
	v_exp_f32_e32 v93, v93
	v_add_f32_e32 v113, v89, v113
	v_exp_f32_e32 v94, v94
	v_add_f32_e32 v113, v90, v113
	v_exp_f32_e32 v95, v95
	v_add_f32_e32 v113, v91, v113
	v_exp_f32_e32 v96, v96
	v_add_f32_e32 v113, v92, v113
	v_exp_f32_e32 v97, v97
	v_add_f32_e32 v113, v93, v113
	v_exp_f32_e32 v98, v98
	v_add_f32_e32 v113, v94, v113
	v_exp_f32_e32 v99, v99
	v_add_f32_e32 v113, v95, v113
	v_exp_f32_e32 v100, v100
	v_add_f32_e32 v113, v96, v113
	v_exp_f32_e32 v101, v101
	v_add_f32_e32 v113, v97, v113
	v_exp_f32_e32 v102, v102
	v_add_f32_e32 v113, v98, v113
	v_exp_f32_e32 v103, v103
	v_add_f32_e32 v113, v99, v113
	v_exp_f32_e32 v104, v104
	v_add_f32_e32 v113, v100, v113
	v_exp_f32_e32 v105, v105
	v_add_f32_e32 v113, v101, v113
	v_exp_f32_e32 v106, v106
	v_add_f32_e32 v113, v102, v113
	v_exp_f32_e32 v107, v107
	v_add_f32_e32 v113, v103, v113
	v_exp_f32_e32 v108, v108
	v_add_f32_e32 v113, v104, v113
	v_exp_f32_e32 v109, v109
	v_add_f32_e32 v113, v105, v113
	v_exp_f32_e32 v110, v110
	v_add_f32_e32 v113, v106, v113
	v_exp_f32_e32 v111, v111
	v_add_f32_e32 v113, v107, v113
	v_exp_f32_e32 v112, v112
	v_add_f32_e32 v113, v108, v113
	v_exp_f32_e32 v17, v17
	v_add_f32_e32 v113, v109, v113
	v_add_f32_e32 v113, v110, v113
	v_add_f32_e32 v113, v111, v113
	v_add_f32_e32 v113, v112, v113
	v_add_f32_e32 v213, v17, v113
	v_mov_b32_e32 v214, v213
	s_nop 1
	v_permlane32_swap_b32_e32 v213, v214
	v_cvt_pk_bf16_f32 v82, v82, v83
	v_cvt_pk_bf16_f32 v83, v84, v85
	v_cvt_pk_bf16_f32 v84, v86, v87
	v_cvt_pk_bf16_f32 v85, v88, v89
	v_cvt_pk_bf16_f32 v86, v90, v91
	v_cvt_pk_bf16_f32 v87, v92, v93
	v_cvt_pk_bf16_f32 v88, v94, v95
	v_cvt_pk_bf16_f32 v89, v96, v97
	v_cvt_pk_bf16_f32 v90, v98, v99
	v_cvt_pk_bf16_f32 v91, v100, v101
	v_cvt_pk_bf16_f32 v92, v102, v103
	v_cvt_pk_bf16_f32 v93, v104, v105
	v_cvt_pk_bf16_f32 v94, v106, v107
	v_cvt_pk_bf16_f32 v95, v108, v109
	v_cvt_pk_bf16_f32 v96, v110, v111
	v_cvt_pk_bf16_f32 v97, v112, v17
	s_nop 0
	v_permlane32_swap_b32_e32 v82, v84
	v_permlane32_swap_b32_e32 v83, v85
	v_permlane32_swap_b32_e32 v86, v88
	v_permlane32_swap_b32_e32 v87, v89
	v_permlane32_swap_b32_e32 v90, v92
	v_permlane32_swap_b32_e32 v91, v93
	v_permlane32_swap_b32_e32 v94, v96
	v_permlane32_swap_b32_e32 v95, v97
	s_waitcnt lgkmcnt(0)
; template <int VB>
; __device__ __forceinline__ void pv_tile(f32x16* o, int vb0, bf16x8 pa0, bf16x8 pa1, bf16x8 pa2, bf16x8 pa3) {
;     ...
;     PV_D0(0); PV_D0(1); PV_D0(2); PV_D0(3);
	ds_read_b64_tr_b16 v[246:247], v181 offset:12800
	ds_read_b64_tr_b16 v[248:249], v181 offset:14848
	ds_read_b64_tr_b16 v[250:251], v181 offset:1024
	ds_read_b64_tr_b16 v[252:253], v181 offset:3072
	ds_read_b64_tr_b16 v[98:99], v181 offset:5120
	ds_read_b64_tr_b16 v[100:101], v181 offset:7168
	ds_read_b64_tr_b16 v[102:103], v181 offset:9216
	ds_read_b64_tr_b16 v[104:105], v181 offset:11264
	ds_read_b64_tr_b16 v[106:107], v181 offset:13312
	ds_read_b64_tr_b16 v[108:109], v181 offset:15360
	ds_read_b64_tr_b16 v[110:111], v181 offset:1536
	ds_read_b64_tr_b16 v[112:113], v181 offset:3584
	v_mfma_f32_32x32x16_bf16 v[66:81], v[82:85], v[218:221], v[66:81]
	ds_read_b64_tr_b16 v[218:219], v181 offset:5632
	ds_read_b64_tr_b16 v[220:221], v181 offset:7680
	v_mfma_f32_32x32x16_bf16 v[66:81], v[86:89], v[222:225], v[66:81]
	s_waitcnt lgkmcnt(13)
	ds_read_b64_tr_b16 v[222:223], v181 offset:9728
	ds_read_b64_tr_b16 v[224:225], v181 offset:11776
	v_mfma_f32_32x32x16_bf16 v[66:81], v[90:93], v[226:229], v[66:81]
	s_waitcnt lgkmcnt(13)
	ds_read_b64_tr_b16 v[226:227], v181 offset:13824
	ds_read_b64_tr_b16 v[228:229], v181 offset:15872
	v_mfma_f32_32x32x16_bf16 v[66:81], v[94:97], v[230:233], v[66:81]
	v_mfma_f32_32x32x16_bf16 v[50:65], v[82:85], v[234:237], v[50:65]
	v_mfma_f32_32x32x16_bf16 v[50:65], v[86:89], v[238:241], v[50:65]
	v_mfma_f32_32x32x16_bf16 v[50:65], v[90:93], v[242:245], v[50:65]
	s_waitcnt lgkmcnt(15)
	v_mfma_f32_32x32x16_bf16 v[50:65], v[94:97], v[246:249], v[50:65]
	s_waitcnt lgkmcnt(14)
	v_mfma_f32_32x32x16_bf16 v[34:49], v[82:85], v[250:253], v[34:49]
	s_waitcnt lgkmcnt(12)
	v_mfma_f32_32x32x16_bf16 v[34:49], v[86:89], v[98:101], v[34:49]
	s_waitcnt lgkmcnt(10)
	v_mfma_f32_32x32x16_bf16 v[34:49], v[90:93], v[102:105], v[34:49]
	s_waitcnt lgkmcnt(8)
	v_mfma_f32_32x32x16_bf16 v[34:49], v[94:97], v[106:109], v[34:49]
	s_waitcnt lgkmcnt(6)
	v_mfma_f32_32x32x16_bf16 v[18:33], v[82:85], v[110:113], v[18:33]
	v_add_u32_e32 v17, s33, v173
	s_waitcnt vmcnt(3)
	ds_write_b128 v17, v[8:11]
	s_waitcnt vmcnt(1)
	ds_write_b128 v17, v[162:165] offset:12288
	v_add_u32_e32 v17, s33, v180
	s_waitcnt vmcnt(0)
	ds_write_b128 v17, v[166:169]
	ds_write_b128 v194, v[4:7] offset:32768
	ds_write_b128 v195, v[12:15] offset:32768
	s_waitcnt lgkmcnt(0)
	s_barrier
	v_mfma_f32_32x32x16_bf16 v[18:33], v[86:89], v[218:221], v[18:33]
	s_add_i32 s4, s86, 6
	s_cmp_lt_u32 s4, s85
	s_cselect_b64 s[66:67], -1, 0
	s_cmp_ge_u32 s4, s85
	v_mfma_f32_32x32x16_bf16 v[18:33], v[90:93], v[222:225], v[18:33]
	v_mfma_f32_32x32x16_bf16 v[18:33], v[94:97], v[226:229], v[18:33]
	s_cbranch_scc1 .LBB0_803
	s_sub_i32 s4, s78, 64
	s_ashr_i32 s5, s4, 31
	s_lshl_b64 s[6:7], s[4:5], 12
	s_add_u32 s6, s76, s6
	s_addc_u32 s7, s77, s7
	v_lshl_add_u64 v[12:13], s[6:7], 0, v[174:175]
	v_add_co_u32_e32 v82, vcc, 0x20000, v12
	v_lshl_add_u64 v[14:15], v[12:13], 0, s[72:73]
	s_nop 0
	v_addc_co_u32_e32 v83, vcc, 0, v13, vcc
	s_lshl_b64 s[4:5], s[4:5], 7
	global_load_dwordx4 v[4:7], v[12:13], off offset:256
	global_load_dwordx4 v[8:11], v[12:13], off
	s_nop 0
	global_load_dwordx4 v[12:15], v[14:15], off offset:256
	s_nop 0
	global_load_dwordx4 v[162:165], v[82:83], off
	v_lshl_add_u64 v[82:83], v[178:179], 0, s[4:5]
	global_load_dwordx4 v[166:169], v[82:83], off

; template <int DQK> __device__ __forceinline__ void partialSM(f32x16& p0, f32x16& p1, float& m_reg, float& mn, float& alpha) {
;     ...
;     for (int r = 0; r < 16; ++r) p0[r] = fmaf(p0[r], C2, mnL);
; #pragma unroll
;     for (int r = 0; r < 16; ++r) p1[r] = fmaf(p1[r], C2, mnL);
; #pragma unroll
;     for (int r = 0; r < 16; ++r) p0[r] = __builtin_amdgcn_exp2f(p0[r]);
; }
; __device__ __forceinline__ void finishSM(f32x16& p0, f32x16& p1, float alpha, float& l_reg, bf16x8& pa0, bf16x8& pa1, bf16x8& pa2, bf16x8& pa3) {
; #pragma unroll
;     for (int r = 0; r < 16; ++r) p1[r] = __builtin_amdgcn_exp2f(p1[r]);
;     float ps = 0;
; #pragma unroll
;     for (int r = 0; r < 16; ++r) ps += p0[r];
; #pragma unroll
;     for (int r = 0; r < 16; ++r) ps += p1[r];
;     { auto rr = __builtin_amdgcn_permlane32_swap(__float_as_uint(ps), __float_as_uint(ps), false, false);
;       ps = __uint_as_float(rr[0]) + __uint_as_float(rr[1]); }
;     l_reg = l_reg * alpha + ps;
;     ...
;     PK4(p0, 0, pa0); PK4(p0, 8, pa1); PK4(p1, 0, pa2); PK4(p1, 8, pa3);
;     ...
; }
; template <int VB>
; __device__ __forceinline__ void pv_tile(f32x16* o, int vb0, bf16x8 pa0, bf16x8 pa1, bf16x8 pa2, bf16x8 pa3) {
;     ...
;     PV_D0(0); PV_D0(1); PV_D0(2); PV_D0(3);
.LBB0_809:
	ds_read_b64_tr_b16 v[220:221], v181 offset:16384
	ds_read_b64_tr_b16 v[222:223], v181 offset:18432
	ds_read_b64_tr_b16 v[224:225], v181 offset:20480
	ds_read_b64_tr_b16 v[226:227], v181 offset:22528
	ds_read_b64_tr_b16 v[228:229], v181 offset:24576
	ds_read_b64_tr_b16 v[230:231], v181 offset:26624
	ds_read_b64_tr_b16 v[232:233], v181 offset:28672
	ds_read_b64_tr_b16 v[234:235], v181 offset:30720
	ds_read_b64_tr_b16 v[236:237], v181 offset:16896
	ds_read_b64_tr_b16 v[238:239], v181 offset:18944
	ds_read_b64_tr_b16 v[240:241], v181 offset:20992
	ds_read_b64_tr_b16 v[242:243], v181 offset:23040
	ds_read_b64_tr_b16 v[244:245], v181 offset:25088
	ds_read_b64_tr_b16 v[246:247], v181 offset:27136
	v_cndmask_b32_e64 v216, v216, v217, s[4:5]
	v_mul_f32_e32 v217, 0xbdd53b94, v216
	v_fmamk_f32 v82, v82, 0x3dd53b94, v217
	v_fmamk_f32 v83, v83, 0x3dd53b94, v217
	v_exp_f32_e32 v82, v82
	v_fmamk_f32 v84, v84, 0x3dd53b94, v217
	v_exp_f32_e32 v83, v83
	v_fmamk_f32 v85, v85, 0x3dd53b94, v217
	v_exp_f32_e32 v84, v84
	v_fmamk_f32 v86, v86, 0x3dd53b94, v217
	v_fmamk_f32 v87, v87, 0x3dd53b94, v217
	v_fmamk_f32 v88, v88, 0x3dd53b94, v217
	v_fmamk_f32 v89, v89, 0x3dd53b94, v217
	v_fmamk_f32 v90, v90, 0x3dd53b94, v217
	v_fmamk_f32 v91, v91, 0x3dd53b94, v217
	v_fmamk_f32 v92, v92, 0x3dd53b94, v217
	v_fmamk_f32 v93, v93, 0x3dd53b94, v217
	v_fmamk_f32 v94, v94, 0x3dd53b94, v217
	v_fmamk_f32 v95, v95, 0x3dd53b94, v217
	v_fmamk_f32 v96, v96, 0x3dd53b94, v217
	v_fmamk_f32 v97, v97, 0x3dd53b94, v217
	v_fmamk_f32 v98, v98, 0x3dd53b94, v217
	v_fmamk_f32 v99, v99, 0x3dd53b94, v217
	v_fmamk_f32 v100, v100, 0x3dd53b94, v217
	v_fmamk_f32 v101, v101, 0x3dd53b94, v217
	v_fmamk_f32 v102, v102, 0x3dd53b94, v217
	v_fmamk_f32 v103, v103, 0x3dd53b94, v217
	v_fmamk_f32 v104, v104, 0x3dd53b94, v217
	v_fmamk_f32 v105, v105, 0x3dd53b94, v217
	v_fmamk_f32 v106, v106, 0x3dd53b94, v217
	v_fmamk_f32 v107, v107, 0x3dd53b94, v217
	v_fmamk_f32 v108, v108, 0x3dd53b94, v217
	v_fmamk_f32 v109, v109, 0x3dd53b94, v217
	v_fmamk_f32 v110, v110, 0x3dd53b94, v217
	v_fmamk_f32 v111, v111, 0x3dd53b94, v217
	v_fmamk_f32 v112, v112, 0x3dd53b94, v217
	v_fmac_f32_e32 v217, 0x3dd53b94, v113
	v_exp_f32_e32 v85, v85
	v_exp_f32_e32 v86, v86
	v_exp_f32_e32 v113, v217
	v_add_f32_e32 v217, 0, v82
	v_exp_f32_e32 v87, v87
	v_add_f32_e32 v217, v83, v217
	v_exp_f32_e32 v88, v88
	v_add_f32_e32 v217, v84, v217
	v_exp_f32_e32 v89, v89
	v_add_f32_e32 v217, v85, v217
	v_exp_f32_e32 v90, v90
	v_add_f32_e32 v217, v86, v217
	v_exp_f32_e32 v91, v91
	v_add_f32_e32 v217, v87, v217
	v_exp_f32_e32 v92, v92
	v_add_f32_e32 v217, v88, v217
	v_exp_f32_e32 v93, v93
	v_add_f32_e32 v217, v89, v217
	v_exp_f32_e32 v94, v94
	v_add_f32_e32 v217, v90, v217
	v_exp_f32_e32 v95, v95
	v_add_f32_e32 v217, v91, v217
	v_exp_f32_e32 v96, v96
	v_add_f32_e32 v217, v92, v217
	v_exp_f32_e32 v97, v97
	v_add_f32_e32 v217, v93, v217
	v_exp_f32_e32 v98, v98
	v_add_f32_e32 v217, v94, v217
	v_exp_f32_e32 v99, v99
	v_add_f32_e32 v217, v95, v217
	v_exp_f32_e32 v100, v100
	v_add_f32_e32 v217, v96, v217
	v_exp_f32_e32 v101, v101
	v_add_f32_e32 v217, v97, v217
	v_exp_f32_e32 v102, v102
	v_add_f32_e32 v217, v98, v217
	v_exp_f32_e32 v103, v103
	v_add_f32_e32 v217, v99, v217
	v_exp_f32_e32 v104, v104
	v_add_f32_e32 v217, v100, v217
	v_exp_f32_e32 v105, v105
	v_add_f32_e32 v217, v101, v217
	v_exp_f32_e32 v106, v106
	v_add_f32_e32 v217, v102, v217
	v_exp_f32_e32 v107, v107
	v_add_f32_e32 v217, v103, v217
	v_exp_f32_e32 v108, v108
	v_add_f32_e32 v217, v104, v217
	v_exp_f32_e32 v109, v109
	v_add_f32_e32 v217, v105, v217
	v_exp_f32_e32 v110, v110
	v_add_f32_e32 v217, v106, v217
	v_exp_f32_e32 v111, v111
	v_add_f32_e32 v217, v107, v217
	v_exp_f32_e32 v112, v112
	v_add_f32_e32 v217, v108, v217
	v_add_f32_e32 v217, v109, v217
	v_add_f32_e32 v217, v110, v217
	v_add_f32_e32 v217, v111, v217
	v_add_f32_e32 v217, v112, v217
	v_add_f32_e32 v217, v113, v217
	v_mov_b32_e32 v218, v217
	s_nop 1
	v_permlane32_swap_b32_e32 v217, v218
	v_cvt_pk_bf16_f32 v82, v82, v83
	v_cvt_pk_bf16_f32 v83, v84, v85
	v_cvt_pk_bf16_f32 v84, v86, v87
	v_cvt_pk_bf16_f32 v85, v88, v89
	v_cvt_pk_bf16_f32 v86, v90, v91
	v_cvt_pk_bf16_f32 v87, v92, v93
	v_cvt_pk_bf16_f32 v88, v94, v95
	v_cvt_pk_bf16_f32 v89, v96, v97
	v_cvt_pk_bf16_f32 v90, v98, v99
	v_cvt_pk_bf16_f32 v91, v100, v101
	v_cvt_pk_bf16_f32 v92, v102, v103
	v_cvt_pk_bf16_f32 v93, v104, v105
	v_cvt_pk_bf16_f32 v94, v106, v107
	v_cvt_pk_bf16_f32 v95, v108, v109
	v_cvt_pk_bf16_f32 v96, v110, v111
	v_cvt_pk_bf16_f32 v97, v112, v113
	s_nop 0
	v_permlane32_swap_b32_e32 v82, v84
	v_permlane32_swap_b32_e32 v83, v85
	v_permlane32_swap_b32_e32 v86, v88
	v_permlane32_swap_b32_e32 v87, v89
	v_permlane32_swap_b32_e32 v90, v92
	v_permlane32_swap_b32_e32 v91, v93
	v_permlane32_swap_b32_e32 v94, v96
	v_permlane32_swap_b32_e32 v95, v97
	s_waitcnt lgkmcnt(0)
; template <int VB>
; __device__ __forceinline__ void pv_tile(f32x16* o, int vb0, bf16x8 pa0, bf16x8 pa1, bf16x8 pa2, bf16x8 pa3) {
;     ...
;     PV_D0(0); PV_D0(1); PV_D0(2); PV_D0(3);
	ds_read_b64_tr_b16 v[248:249], v181 offset:29184
	ds_read_b64_tr_b16 v[250:251], v181 offset:31232
	ds_read_b64_tr_b16 v[98:99], v181 offset:17408
	ds_read_b64_tr_b16 v[100:101], v181 offset:19456
	ds_read_b64_tr_b16 v[102:103], v181 offset:21504
	ds_read_b64_tr_b16 v[104:105], v181 offset:23552
	ds_read_b64_tr_b16 v[106:107], v181 offset:25600
	ds_read_b64_tr_b16 v[108:109], v181 offset:27648
	ds_read_b64_tr_b16 v[110:111], v181 offset:29696
	ds_read_b64_tr_b16 v[112:113], v181 offset:31744
	v_mfma_f32_32x32x16_bf16 v[66:81], v[82:85], v[220:223], v[66:81]
	ds_read_b64_tr_b16 v[220:221], v181 offset:17920
	ds_read_b64_tr_b16 v[222:223], v181 offset:19968
	v_mfma_f32_32x32x16_bf16 v[66:81], v[86:89], v[224:227], v[66:81]
	ds_read_b64_tr_b16 v[224:225], v181 offset:22016
	ds_read_b64_tr_b16 v[226:227], v181 offset:24064
	v_mfma_f32_32x32x16_bf16 v[66:81], v[90:93], v[228:231], v[66:81]
	s_waitcnt lgkmcnt(13)
	ds_read_b64_tr_b16 v[228:229], v181 offset:26112
	ds_read_b64_tr_b16 v[230:231], v181 offset:28160
	v_mfma_f32_32x32x16_bf16 v[66:81], v[94:97], v[232:235], v[66:81]
	s_waitcnt lgkmcnt(13)
	ds_read_b64_tr_b16 v[232:233], v181 offset:30208
	ds_read_b64_tr_b16 v[234:235], v181 offset:32256
	v_mfma_f32_32x32x16_bf16 v[50:65], v[82:85], v[236:239], v[50:65]
	v_mfma_f32_32x32x16_bf16 v[50:65], v[86:89], v[240:243], v[50:65]
	v_mfma_f32_32x32x16_bf16 v[50:65], v[90:93], v[244:247], v[50:65]
	s_waitcnt lgkmcnt(15)
	v_mfma_f32_32x32x16_bf16 v[50:65], v[94:97], v[248:251], v[50:65]
	s_waitcnt lgkmcnt(14)
	v_mfma_f32_32x32x16_bf16 v[34:49], v[82:85], v[98:101], v[34:49]
	s_waitcnt lgkmcnt(12)
	v_mfma_f32_32x32x16_bf16 v[34:49], v[86:89], v[102:105], v[34:49]
	s_waitcnt lgkmcnt(10)
	v_mfma_f32_32x32x16_bf16 v[34:49], v[90:93], v[106:109], v[34:49]
	s_waitcnt lgkmcnt(8)
	v_mfma_f32_32x32x16_bf16 v[34:49], v[94:97], v[110:113], v[34:49]
	s_waitcnt lgkmcnt(6)
	v_mfma_f32_32x32x16_bf16 v[18:33], v[82:85], v[220:223], v[18:33]
	v_cndmask_b32_e64 v82, 0, 1, s[66:67]
	v_cmp_ne_u32_e64 s[4:5], 1, v82
	s_andn2_b64 vcc, exec, s[66:67]
	s_waitcnt lgkmcnt(4)
	v_mfma_f32_32x32x16_bf16 v[18:33], v[86:89], v[224:227], v[18:33]
	s_waitcnt lgkmcnt(2)
	v_mfma_f32_32x32x16_bf16 v[18:33], v[90:93], v[228:231], v[18:33]
	s_waitcnt lgkmcnt(0)
	v_mfma_f32_32x32x16_bf16 v[18:33], v[94:97], v[232:235], v[18:33]
	s_cbranch_vccnz .LBB0_811
	s_waitcnt vmcnt(3)
	ds_write_b128 v192, v[8:11] offset:49152
	s_waitcnt vmcnt(1)
	ds_write_b128 v192, v[162:165] offset:61440
	s_waitcnt vmcnt(0)
	ds_write_b128 v193, v[166:169] offset:49408
	ds_write_b128 v194, v[4:7]
	ds_write_b128 v195, v[12:15]

; template <int DQK> __device__ __forceinline__ void partialSM(f32x16& p0, f32x16& p1, float& m_reg, float& mn, float& alpha) {
;     ...
;     for (int r = 0; r < 16; ++r) p0[r] = fmaf(p0[r], C2, mnL);
; #pragma unroll
;     for (int r = 0; r < 16; ++r) p1[r] = fmaf(p1[r], C2, mnL);
; #pragma unroll
;     for (int r = 0; r < 16; ++r) p0[r] = __builtin_amdgcn_exp2f(p0[r]);
; }
; __device__ __forceinline__ void finishSM(f32x16& p0, f32x16& p1, float alpha, float& l_reg, bf16x8& pa0, bf16x8& pa1, bf16x8& pa2, bf16x8& pa3) {
; #pragma unroll
;     for (int r = 0; r < 16; ++r) p1[r] = __builtin_amdgcn_exp2f(p1[r]);
;     float ps = 0;
; #pragma unroll
;     for (int r = 0; r < 16; ++r) ps += p0[r];
; #pragma unroll
;     for (int r = 0; r < 16; ++r) ps += p1[r];
;     { auto rr = __builtin_amdgcn_permlane32_swap(__float_as_uint(ps), __float_as_uint(ps), false, false);
;       ps = __uint_as_float(rr[0]) + __uint_as_float(rr[1]); }
;     l_reg = l_reg * alpha + ps;
;     ...
;     PK4(p0, 0, pa0); PK4(p0, 8, pa1); PK4(p1, 0, pa2); PK4(p1, 8, pa3);
;     ...
; }
.LBB0_819:
	ds_read_b64_tr_b16 v[236:237], v181 offset:32768
	ds_read_b64_tr_b16 v[238:239], v181 offset:34816
	ds_read_b64_tr_b16 v[240:241], v181 offset:36864
	ds_read_b64_tr_b16 v[242:243], v181 offset:38912
	ds_read_b64_tr_b16 v[244:245], v181 offset:40960
	ds_read_b64_tr_b16 v[246:247], v181 offset:43008
	ds_read_b64_tr_b16 v[248:249], v181 offset:45056
	ds_read_b64_tr_b16 v[250:251], v181 offset:47104
	v_cndmask_b32_e64 v216, v216, v220, s[6:7]
	v_mul_f32_e32 v220, 0xbdd53b94, v216
	v_fmamk_f32 v98, v98, 0x3dd53b94, v220
	v_fmamk_f32 v99, v99, 0x3dd53b94, v220
	v_fmamk_f32 v100, v100, 0x3dd53b94, v220
	v_fmamk_f32 v101, v101, 0x3dd53b94, v220
	v_fmamk_f32 v102, v102, 0x3dd53b94, v220
	v_fmamk_f32 v103, v103, 0x3dd53b94, v220
	v_fmamk_f32 v104, v104, 0x3dd53b94, v220
	v_fmamk_f32 v105, v105, 0x3dd53b94, v220
	v_fmamk_f32 v106, v106, 0x3dd53b94, v220
	v_fmamk_f32 v107, v107, 0x3dd53b94, v220
	v_fmamk_f32 v108, v108, 0x3dd53b94, v220
	v_fmamk_f32 v109, v109, 0x3dd53b94, v220
	v_fmamk_f32 v110, v110, 0x3dd53b94, v220
	v_fmamk_f32 v111, v111, 0x3dd53b94, v220
	v_fmamk_f32 v112, v112, 0x3dd53b94, v220
	v_fmamk_f32 v113, v113, 0x3dd53b94, v220
	v_fmamk_f32 v82, v82, 0x3dd53b94, v220
	v_fmamk_f32 v83, v83, 0x3dd53b94, v220
	v_fmamk_f32 v84, v84, 0x3dd53b94, v220
	v_fmamk_f32 v85, v85, 0x3dd53b94, v220
	v_fmamk_f32 v86, v86, 0x3dd53b94, v220
	v_fmamk_f32 v87, v87, 0x3dd53b94, v220
	v_fmamk_f32 v88, v88, 0x3dd53b94, v220
	v_fmamk_f32 v89, v89, 0x3dd53b94, v220
	v_fmamk_f32 v90, v90, 0x3dd53b94, v220
	v_fmamk_f32 v91, v91, 0x3dd53b94, v220
	v_fmamk_f32 v92, v92, 0x3dd53b94, v220
	v_fmamk_f32 v93, v93, 0x3dd53b94, v220
	v_fmamk_f32 v94, v94, 0x3dd53b94, v220
	v_fmamk_f32 v95, v95, 0x3dd53b94, v220
	v_fmamk_f32 v96, v96, 0x3dd53b94, v220
	v_fmac_f32_e32 v220, 0x3dd53b94, v97
	v_exp_f32_e32 v97, v98
	v_exp_f32_e32 v98, v99
	v_exp_f32_e32 v99, v100
	v_exp_f32_e32 v100, v101
	v_exp_f32_e32 v101, v102
	v_exp_f32_e32 v102, v103
	v_exp_f32_e32 v103, v104
	v_exp_f32_e32 v104, v105
	v_exp_f32_e32 v105, v106
	v_exp_f32_e32 v106, v107
	v_exp_f32_e32 v107, v108
	v_exp_f32_e32 v108, v109
	v_exp_f32_e32 v109, v110
	v_exp_f32_e32 v110, v111
	v_exp_f32_e32 v111, v112
	v_exp_f32_e32 v112, v113
	v_exp_f32_e32 v113, v82
	v_add_f32_e32 v82, 0, v97
	v_add_f32_e32 v82, v98, v82
	v_add_f32_e32 v82, v99, v82
	v_add_f32_e32 v82, v100, v82
	v_add_f32_e32 v82, v101, v82
	v_add_f32_e32 v82, v102, v82
	v_add_f32_e32 v82, v103, v82
	v_add_f32_e32 v82, v104, v82
	v_add_f32_e32 v82, v105, v82
	v_add_f32_e32 v82, v106, v82
	v_add_f32_e32 v82, v107, v82
	v_add_f32_e32 v82, v108, v82
	v_add_f32_e32 v82, v109, v82
	v_exp_f32_e32 v221, v83
	v_add_f32_e32 v82, v110, v82
	v_exp_f32_e32 v222, v84
	v_add_f32_e32 v82, v111, v82
	v_exp_f32_e32 v223, v85
	v_add_f32_e32 v82, v112, v82
	v_exp_f32_e32 v224, v86
	v_add_f32_e32 v82, v113, v82
	v_exp_f32_e32 v225, v87
	v_add_f32_e32 v82, v221, v82
	v_exp_f32_e32 v226, v88
	v_add_f32_e32 v82, v222, v82
	v_exp_f32_e32 v227, v89
	v_add_f32_e32 v82, v223, v82
	v_exp_f32_e32 v228, v90
	v_add_f32_e32 v82, v224, v82
	v_exp_f32_e32 v229, v91
	v_add_f32_e32 v82, v225, v82
	v_exp_f32_e32 v230, v92
	v_add_f32_e32 v82, v226, v82
	v_exp_f32_e32 v231, v93
	v_add_f32_e32 v82, v227, v82
	v_exp_f32_e32 v232, v94
	v_add_f32_e32 v82, v228, v82
	v_exp_f32_e32 v233, v95
	v_add_f32_e32 v82, v229, v82
	v_exp_f32_e32 v234, v96
	v_add_f32_e32 v82, v230, v82
	v_exp_f32_e32 v220, v220
	v_add_f32_e32 v82, v231, v82
	v_add_f32_e32 v82, v232, v82
	v_add_f32_e32 v82, v233, v82
	v_add_f32_e32 v82, v234, v82
	v_add_f32_e32 v82, v220, v82
	v_mov_b32_e32 v83, v82
	s_nop 1
	v_permlane32_swap_b32_e32 v82, v83
	v_cvt_pk_bf16_f32 v84, v97, v98
	v_cvt_pk_bf16_f32 v85, v99, v100
	v_cvt_pk_bf16_f32 v86, v101, v102
	v_cvt_pk_bf16_f32 v87, v103, v104
	v_cvt_pk_bf16_f32 v88, v105, v106
	v_cvt_pk_bf16_f32 v89, v107, v108
	v_cvt_pk_bf16_f32 v90, v109, v110
	v_cvt_pk_bf16_f32 v91, v111, v112
	v_cvt_pk_bf16_f32 v92, v113, v221
	v_cvt_pk_bf16_f32 v93, v222, v223
	v_cvt_pk_bf16_f32 v94, v224, v225
	v_cvt_pk_bf16_f32 v95, v226, v227
	v_cvt_pk_bf16_f32 v96, v228, v229
	v_cvt_pk_bf16_f32 v97, v230, v231
	v_cvt_pk_bf16_f32 v98, v232, v233
	v_cvt_pk_bf16_f32 v99, v234, v220
	s_nop 0
	v_permlane32_swap_b32_e32 v84, v86
	v_permlane32_swap_b32_e32 v85, v87
	v_permlane32_swap_b32_e32 v88, v90
	v_permlane32_swap_b32_e32 v89, v91
	v_permlane32_swap_b32_e32 v92, v94
	v_permlane32_swap_b32_e32 v93, v95
	v_permlane32_swap_b32_e32 v96, v98
	v_permlane32_swap_b32_e32 v97, v99
	s_waitcnt lgkmcnt(0)
; template <int VB>
; __device__ __forceinline__ void pv_tile(f32x16* o, int vb0, bf16x8 pa0, bf16x8 pa1, bf16x8 pa2, bf16x8 pa3) {
;     ...
;     PV_D0(0); PV_D0(1); PV_D0(2); PV_D0(3);
; template <int DQK, bool BIAS> ...
;     ...
;     int t = 0;
;     for (; t + 2 < NT; t += 3) { A_STEP(t, 0); A_STEP(t + 1, 1); A_STEP(t + 2, 2); }
	ds_read_b64_tr_b16 v[220:221], v181 offset:33280
	ds_read_b64_tr_b16 v[222:223], v181 offset:35328
	ds_read_b64_tr_b16 v[224:225], v181 offset:37376
	ds_read_b64_tr_b16 v[226:227], v181 offset:39424
	ds_read_b64_tr_b16 v[228:229], v181 offset:41472
	ds_read_b64_tr_b16 v[230:231], v181 offset:43520
	ds_read_b64_tr_b16 v[232:233], v181 offset:45568
	ds_read_b64_tr_b16 v[234:235], v181 offset:47616
	ds_read_b64_tr_b16 v[100:101], v181 offset:33792
	ds_read_b64_tr_b16 v[102:103], v181 offset:35840
	ds_read_b64_tr_b16 v[104:105], v181 offset:37888
	ds_read_b64_tr_b16 v[106:107], v181 offset:39936
	ds_read_b64_tr_b16 v[108:109], v181 offset:41984
	ds_read_b64_tr_b16 v[110:111], v181 offset:44032
	v_mfma_f32_32x32x16_bf16 v[66:81], v[84:87], v[236:239], v[66:81]
	s_waitcnt lgkmcnt(13)
	ds_read_b64_tr_b16 v[236:237], v181 offset:46080
	ds_read_b64_tr_b16 v[238:239], v181 offset:48128
	v_mfma_f32_32x32x16_bf16 v[66:81], v[88:91], v[240:243], v[66:81]
	s_waitcnt lgkmcnt(13)
	ds_read_b64_tr_b16 v[240:241], v181 offset:34304
	ds_read_b64_tr_b16 v[242:243], v181 offset:36352
	v_mfma_f32_32x32x16_bf16 v[66:81], v[92:95], v[244:247], v[66:81]
	s_waitcnt lgkmcnt(13)
	ds_read_b64_tr_b16 v[244:245], v181 offset:38400
	ds_read_b64_tr_b16 v[246:247], v181 offset:40448
	v_mfma_f32_32x32x16_bf16 v[66:81], v[96:99], v[248:251], v[66:81]
	s_waitcnt lgkmcnt(13)
	ds_read_b64_tr_b16 v[248:249], v181 offset:42496
	ds_read_b64_tr_b16 v[250:251], v181 offset:44544
	s_waitcnt lgkmcnt(15)
	v_mfma_f32_32x32x16_bf16 v[50:65], v[84:87], v[220:223], v[50:65]
	s_waitcnt lgkmcnt(13)
	ds_read_b64_tr_b16 v[220:221], v181 offset:46592
	ds_read_b64_tr_b16 v[222:223], v181 offset:48640
	s_waitcnt lgkmcnt(15)
	v_mfma_f32_32x32x16_bf16 v[50:65], v[88:91], v[224:227], v[50:65]
	s_waitcnt lgkmcnt(15)
	v_mfma_f32_32x32x16_bf16 v[50:65], v[92:95], v[228:231], v[50:65]
	s_waitcnt lgkmcnt(15)
	v_mfma_f32_32x32x16_bf16 v[50:65], v[96:99], v[232:235], v[50:65]
	s_waitcnt lgkmcnt(14)
	v_mfma_f32_32x32x16_bf16 v[34:49], v[84:87], v[100:103], v[34:49]
	s_waitcnt lgkmcnt(12)
	v_mfma_f32_32x32x16_bf16 v[34:49], v[88:91], v[104:107], v[34:49]
	s_waitcnt lgkmcnt(10)
	v_mfma_f32_32x32x16_bf16 v[34:49], v[92:95], v[108:111], v[34:49]
	s_waitcnt lgkmcnt(8)
	v_mfma_f32_32x32x16_bf16 v[34:49], v[96:99], v[236:239], v[34:49]
	s_waitcnt lgkmcnt(6)
	v_mfma_f32_32x32x16_bf16 v[18:33], v[84:87], v[240:243], v[18:33]
	s_andn2_b64 vcc, exec, s[80:81]
	s_waitcnt lgkmcnt(4)
	v_mfma_f32_32x32x16_bf16 v[18:33], v[88:91], v[244:247], v[18:33]
	s_waitcnt lgkmcnt(2)
	v_mfma_f32_32x32x16_bf16 v[18:33], v[92:95], v[248:251], v[18:33]
	s_waitcnt lgkmcnt(0)
	v_mfma_f32_32x32x16_bf16 v[18:33], v[96:99], v[220:223], v[18:33]
	s_cbranch_vccnz .LBB0_794
	s_waitcnt vmcnt(3)
	ds_write_b128 v196, v[8:11]
	s_waitcnt vmcnt(1)
	ds_write_b128 v196, v[162:165] offset:12288
	s_waitcnt vmcnt(0)
	ds_write_b128 v197, v[166:169]
	ds_write_b128 v194, v[4:7] offset:16384
	ds_write_b128 v195, v[12:15] offset:16384
	s_branch .LBB0_794

; __global__ void __launch_bounds__(NWAVES * 64, 2) fwd_kernel(Args args) {
;     extern __shared__ __attribute__((aligned(16))) unsigned char lds_raw[];
	.amdhsa_kernel _Z10fwd_kernel4Args
		.amdhsa_group_segment_fixed_size 0
		.amdhsa_private_segment_fixed_size 0
		.amdhsa_kernarg_size 424
		.amdhsa_user_sgpr_count 2
		.amdhsa_user_sgpr_dispatch_ptr 0
		.amdhsa_user_sgpr_queue_ptr 0
		.amdhsa_user_sgpr_kernarg_segment_ptr 1
		.amdhsa_user_sgpr_dispatch_id 0
		.amdhsa_user_sgpr_kernarg_preload_length 0
		.amdhsa_user_sgpr_kernarg_preload_offset 0
		.amdhsa_user_sgpr_private_segment_size 0
		.amdhsa_uses_dynamic_stack 0
		.amdhsa_enable_private_segment 0
		.amdhsa_system_sgpr_workgroup_id_x 1
		.amdhsa_system_sgpr_workgroup_id_y 0
		.amdhsa_system_sgpr_workgroup_id_z 0
		.amdhsa_system_sgpr_workgroup_info 0
		.amdhsa_system_vgpr_workitem_id 0
		.amdhsa_next_free_vgpr 256
		.amdhsa_next_free_sgpr 98
		.amdhsa_accum_offset 256
		.amdhsa_reserve_vcc 1
		.amdhsa_float_round_mode_32 0
		.amdhsa_float_round_mode_16_64 0
		.amdhsa_float_denorm_mode_32 3
		.amdhsa_float_denorm_mode_16_64 3
		.amdhsa_dx10_clamp 1
		.amdhsa_ieee_mode 1
		.amdhsa_fp16_overflow 0
		.amdhsa_tg_split 0
		.amdhsa_exception_fp_ieee_invalid_op 0
		.amdhsa_exception_fp_denorm_src 0
		.amdhsa_exception_fp_ieee_div_zero 0
		.amdhsa_exception_fp_ieee_overflow 0
		.amdhsa_exception_fp_ieee_underflow 0
		.amdhsa_exception_fp_ieee_inexact 0
		.amdhsa_exception_int_div_zero 0
	.end_amdhsa_kernel

; __global__ void __launch_bounds__(NWAVES * 64, 2) fwd_kernel(Args args) {
;     extern __shared__ __attribute__((aligned(16))) unsigned char lds_raw[];
amdhsa.kernels:
  - .agpr_count:     0
    .args:
      - .offset:         0
        .size:           168
        .value_kind:     by_value
      - .offset:         168
        .size:           4
        .value_kind:     hidden_block_count_x
      - .offset:         172
        .size:           4
        .value_kind:     hidden_block_count_y
      - .offset:         176
        .size:           4
        .value_kind:     hidden_block_count_z
      - .offset:         180
        .size:           2
        .value_kind:     hidden_group_size_x
      - .offset:         182
        .size:           2
        .value_kind:     hidden_group_size_y
      - .offset:         184
        .size:           2
        .value_kind:     hidden_group_size_z
      - .offset:         186
        .size:           2
        .value_kind:     hidden_remainder_x
      - .offset:         188
        .size:           2
        .value_kind:     hidden_remainder_y
      - .offset:         190
        .size:           2
        .value_kind:     hidden_remainder_z
      - .offset:         208
        .size:           8
        .value_kind:     hidden_global_offset_x
      - .offset:         216
        .size:           8
        .value_kind:     hidden_global_offset_y
      - .offset:         224
        .size:           8
        .value_kind:     hidden_global_offset_z
      - .offset:         232
        .size:           2
        .value_kind:     hidden_grid_dims
      - .offset:         288
        .size:           4
        .value_kind:     hidden_dynamic_lds_size
    .group_segment_fixed_size: 0
    .kernarg_segment_align: 8
    .kernarg_segment_size: 424
    .language:       OpenCL C
    .language_version:
      - 2
      - 0
    .max_flat_workgroup_size: 512
    .name:           _Z10fwd_kernel4Args
    .private_segment_fixed_size: 0
    .sgpr_count:     104
    .sgpr_spill_count: 96
    .symbol:         _Z10fwd_kernel4Args.kd
    .uniform_work_group_size: 1
    .uses_dynamic_stack: false
    .vgpr_count:     256
    .vgpr_spill_count: 0
    .wavefront_size: 64
